# baseline (speedup 1.0000x reference)
.LBB1_24:
	v_add_u32_e32 v190, s27, v188
	ds_read_b64_tr_b16 v[196:197], v190 offset:24576
	ds_read_b64_tr_b16 v[198:199], v190 offset:25088
	v_add_f32_e32 v88, v68, v69
	v_add_f32_e32 v88, v70, v88
	v_add_f32_e32 v88, v71, v88
	v_add_f32_e32 v88, v72, v88
	v_add_f32_e32 v88, v73, v88
	v_cvt_pk_bf16_f32 v160, v68, v69
	v_cvt_pk_bf16_f32 v161, v70, v71
	s_waitcnt lgkmcnt(9)
	v_mfma_f32_32x32x16_bf16 v[100:115], v[84:87], v[144:147], v[36:51]
	ds_read_b64_tr_b16 v[68:69], v190 offset:28672
	ds_read_b64_tr_b16 v[70:71], v190 offset:29184
	v_add_f32_e32 v84, v74, v88
	v_add_f32_e32 v84, v75, v84
	v_add_f32_e32 v84, v76, v84
	v_add_f32_e32 v148, v77, v84
	s_waitcnt lgkmcnt(10)
	v_mfma_f32_32x32x16_bf16 v[84:99], v[172:175], v[144:147], v[36:51]
	v_cvt_pk_bf16_f32 v162, v72, v73
	v_cvt_pk_bf16_f32 v163, v74, v75
	ds_read_b64_tr_b16 v[72:73], v190 offset:25600
	ds_read_b64_tr_b16 v[74:75], v190 offset:26112
	v_add_f32_e32 v148, v78, v148
	v_add_f32_e32 v148, v79, v148
	v_add_f32_e32 v148, v80, v148
	v_add_f32_e32 v148, v81, v148
	v_cvt_pk_bf16_f32 v156, v76, v77
	v_cvt_pk_bf16_f32 v157, v78, v79
	s_waitcnt lgkmcnt(11)
	v_mfma_f32_32x32x16_bf16 v[100:115], v[168:171], v[140:143], v[100:115]
	ds_read_b64_tr_b16 v[76:77], v190 offset:29696
	ds_read_b64_tr_b16 v[78:79], v190 offset:30208
	s_waitcnt lgkmcnt(12)
	v_mfma_f32_32x32x16_bf16 v[84:99], v[164:167], v[140:143], v[84:99]
	v_add_f32_e32 v148, v82, v148
	v_add_f32_e32 v148, v83, v148
	v_add_f32_e32 v148, v52, v148
	v_add_f32_e32 v148, v53, v148
	v_cvt_pk_bf16_f32 v158, v80, v81
	v_cvt_pk_bf16_f32 v159, v82, v83
	ds_read_b64_tr_b16 v[80:81], v190 offset:26624
	ds_read_b64_tr_b16 v[82:83], v190 offset:27136
	v_add_f32_e32 v148, v54, v148
	v_add_f32_e32 v148, v55, v148
	v_add_f32_e32 v148, v56, v148
	v_add_f32_e32 v148, v57, v148
	v_cvt_pk_bf16_f32 v152, v52, v53
	v_cvt_pk_bf16_f32 v153, v54, v55
	s_waitcnt lgkmcnt(13)
	v_mfma_f32_32x32x16_bf16 v[100:115], v[128:131], v[132:135], v[100:115]
	ds_read_b64_tr_b16 v[52:53], v190 offset:30720
	ds_read_b64_tr_b16 v[54:55], v190 offset:31232
	s_waitcnt lgkmcnt(14)
	v_mfma_f32_32x32x16_bf16 v[84:99], v[124:127], v[132:135], v[84:99]
	v_add_f32_e32 v128, v58, v148
	v_add_f32_e32 v128, v59, v128
	v_add_f32_e32 v128, v60, v128
	v_add_f32_e32 v128, v61, v128
	v_cvt_pk_bf16_f32 v154, v56, v57
	v_cvt_pk_bf16_f32 v155, v58, v59
	ds_read_b64_tr_b16 v[56:57], v190 offset:27648
	ds_read_b64_tr_b16 v[58:59], v190 offset:28160
	v_add_f32_e32 v124, v62, v128
	v_add_f32_e32 v124, v63, v124
	v_add_f32_e32 v124, v64, v124
	v_add_f32_e32 v124, v65, v124
	v_cvt_pk_bf16_f32 v148, v60, v61
	v_cvt_pk_bf16_f32 v149, v62, v63
	s_waitcnt lgkmcnt(14)
	v_mfma_f32_32x32x16_bf16 v[100:115], v[120:123], v[136:139], v[100:115]
	ds_read_b64_tr_b16 v[60:61], v190 offset:31744
	ds_read_b64_tr_b16 v[62:63], v190 offset:32256
	v_mfma_f32_32x32x16_bf16 v[84:99], v[116:119], v[136:139], v[84:99]
	v_add_f32_e32 v120, v66, v124
	v_add_f32_e32 v120, v67, v120
	v_add_f32_e32 v190, 0, v120
	v_cvt_pk_bf16_f32 v150, v64, v65
	v_cvt_pk_bf16_f32 v151, v66, v67
	v_lshl_add_u64 v[64:65], v[182:183], 0, s[6:7]
	s_add_i32 s27, s73, s70
	s_mov_b32 s74, m0
	s_mov_b32 m0, s27
	s_nop 0
	global_load_lds_dwordx4 v[64:65], off
	s_mov_b32 m0, s74
	v_lshl_add_u64 v[64:65], v[184:185], 0, s[2:3]
	s_add_i32 s27, s72, s69
	s_mov_b32 s74, m0
	s_mov_b32 m0, s27
	s_nop 0
	global_load_lds_dwordx4 v[64:65], off
	s_mov_b32 m0, s74
	s_waitcnt lgkmcnt(14)
	v_mfma_f32_32x32x16_bf16 v[4:19], v[160:163], v[196:199], v[4:19]
	v_exp_f32_e32 v100, v100
	v_exp_f32_e32 v101, v101
	v_exp_f32_e32 v102, v102
	v_exp_f32_e32 v103, v103
	s_waitcnt lgkmcnt(12)
	v_mfma_f32_32x32x16_bf16 v[20:35], v[160:163], v[68:71], v[20:35]
	v_exp_f32_e32 v104, v104
	v_exp_f32_e32 v105, v105
	v_exp_f32_e32 v106, v106
	v_exp_f32_e32 v107, v107
	v_add_u32_e32 v68, s72, v189
	ds_read_b128 v[64:67], v68
	ds_read_b128 v[116:119], v68 offset:512
	s_waitcnt lgkmcnt(12)
	v_mfma_f32_32x32x16_bf16 v[4:19], v[156:159], v[72:75], v[4:19]
	v_exp_f32_e32 v108, v108
	v_exp_f32_e32 v109, v109
	v_exp_f32_e32 v110, v110
	v_exp_f32_e32 v111, v111
	ds_read_b128 v[120:123], v68 offset:2048
	ds_read_b128 v[124:127], v68 offset:2560
	s_waitcnt lgkmcnt(12)
	v_mfma_f32_32x32x16_bf16 v[20:35], v[156:159], v[76:79], v[20:35]
	v_exp_f32_e32 v112, v112
	v_exp_f32_e32 v113, v113
	v_exp_f32_e32 v114, v114
	v_exp_f32_e32 v115, v115
	ds_read_b128 v[128:131], v68 offset:4096
	ds_read_b128 v[164:167], v68 offset:4608
	s_waitcnt lgkmcnt(12)
	v_mfma_f32_32x32x16_bf16 v[4:19], v[152:155], v[80:83], v[4:19]
	v_exp_f32_e32 v84, v84
	v_exp_f32_e32 v85, v85
	v_exp_f32_e32 v86, v86
	v_exp_f32_e32 v87, v87
	ds_read_b128 v[168:171], v68 offset:6144
	ds_read_b128 v[172:175], v68 offset:6656
	s_waitcnt lgkmcnt(12)
	v_mfma_f32_32x32x16_bf16 v[20:35], v[152:155], v[52:55], v[20:35]
	v_exp_f32_e32 v88, v88
	v_exp_f32_e32 v89, v89
	v_exp_f32_e32 v90, v90
	v_exp_f32_e32 v91, v91
	s_waitcnt lgkmcnt(10)
	v_mfma_f32_32x32x16_bf16 v[4:19], v[148:151], v[56:59], v[4:19]
	v_exp_f32_e32 v92, v92
	v_exp_f32_e32 v93, v93
	v_exp_f32_e32 v94, v94
	v_exp_f32_e32 v95, v95
	s_waitcnt lgkmcnt(8)
	v_mfma_f32_32x32x16_bf16 v[20:35], v[148:151], v[60:63], v[20:35]
	v_exp_f32_e32 v96, v96
	v_exp_f32_e32 v97, v97
	v_exp_f32_e32 v98, v98
	v_exp_f32_e32 v99, v99
	s_waitcnt vmcnt(2) lgkmcnt(0)
	s_barrier
	s_add_i32 s27, s72, 0x2000
	s_cmpk_lg_i32 s72, 0x4000
	s_cselect_b32 s74, s27, 0
	v_add_u32_e32 v191, s73, v188
	ds_read_b64_tr_b16 v[196:197], v191 offset:24576
	ds_read_b64_tr_b16 v[198:199], v191 offset:25088
	s_waitcnt lgkmcnt(9)
	v_mfma_f32_32x32x16_bf16 v[68:83], v[64:67], v[144:147], v[36:51]
	v_add_f32_e32 v52, v100, v101
	v_add_f32_e32 v52, v102, v52
	v_add_f32_e32 v52, v103, v52
	v_add_f32_e32 v52, v104, v52
	v_add_f32_e32 v52, v105, v52
	v_cvt_pk_bf16_f32 v160, v100, v101
	v_cvt_pk_bf16_f32 v161, v102, v103
	ds_read_b64_tr_b16 v[100:101], v191 offset:28672
	ds_read_b64_tr_b16 v[102:103], v191 offset:29184
	v_add_f32_e32 v52, v106, v52
	v_add_f32_e32 v52, v107, v52
	v_add_f32_e32 v52, v108, v52
	v_add_f32_e32 v148, v109, v52
	s_waitcnt lgkmcnt(10)
	v_mfma_f32_32x32x16_bf16 v[52:67], v[116:119], v[144:147], v[36:51]
	v_cvt_pk_bf16_f32 v162, v104, v105
	v_cvt_pk_bf16_f32 v163, v106, v107
	ds_read_b64_tr_b16 v[104:105], v191 offset:25600
	ds_read_b64_tr_b16 v[106:107], v191 offset:26112
	s_waitcnt lgkmcnt(11)
	v_mfma_f32_32x32x16_bf16 v[68:83], v[120:123], v[140:143], v[68:83]
	v_add_f32_e32 v116, v110, v148
	v_add_f32_e32 v116, v111, v116
	v_add_f32_e32 v116, v112, v116
	v_add_f32_e32 v116, v113, v116
	v_cvt_pk_bf16_f32 v156, v108, v109
	v_cvt_pk_bf16_f32 v157, v110, v111
	ds_read_b64_tr_b16 v[108:109], v191 offset:29696
	ds_read_b64_tr_b16 v[110:111], v191 offset:30208
	s_waitcnt lgkmcnt(12)
	v_mfma_f32_32x32x16_bf16 v[52:67], v[124:127], v[140:143], v[52:67]
	v_add_f32_e32 v116, v114, v116
	v_add_f32_e32 v116, v115, v116
	v_add_f32_e32 v116, v84, v116
	v_add_f32_e32 v116, v85, v116
	v_cvt_pk_bf16_f32 v158, v112, v113
	v_cvt_pk_bf16_f32 v159, v114, v115
	ds_read_b64_tr_b16 v[112:113], v191 offset:26624
	ds_read_b64_tr_b16 v[114:115], v191 offset:27136
	s_waitcnt lgkmcnt(13)
	v_mfma_f32_32x32x16_bf16 v[68:83], v[128:131], v[132:135], v[68:83]
	v_add_f32_e32 v116, v86, v116
	v_add_f32_e32 v116, v87, v116
	v_add_f32_e32 v116, v88, v116
	v_add_f32_e32 v116, v89, v116
	v_cvt_pk_bf16_f32 v152, v84, v85
	v_cvt_pk_bf16_f32 v153, v86, v87
	ds_read_b64_tr_b16 v[208:209], v191 offset:30720
	ds_read_b64_tr_b16 v[210:211], v191 offset:31232
	s_waitcnt lgkmcnt(14)
	v_mfma_f32_32x32x16_bf16 v[52:67], v[164:167], v[132:135], v[52:67]
	v_add_f32_e32 v84, v90, v116
	v_add_f32_e32 v84, v91, v84
	v_add_f32_e32 v84, v92, v84
	v_add_f32_e32 v84, v93, v84
	v_cvt_pk_bf16_f32 v154, v88, v89
	v_cvt_pk_bf16_f32 v155, v90, v91
	ds_read_b64_tr_b16 v[88:89], v191 offset:27648
	ds_read_b64_tr_b16 v[90:91], v191 offset:28160
	s_waitcnt lgkmcnt(14)
	v_mfma_f32_32x32x16_bf16 v[68:83], v[168:171], v[136:139], v[68:83]
	v_add_f32_e32 v84, v94, v84
	v_add_f32_e32 v84, v95, v84
	v_add_f32_e32 v84, v96, v84
	v_add_f32_e32 v84, v97, v84
	v_cvt_pk_bf16_f32 v148, v92, v93
	v_cvt_pk_bf16_f32 v149, v94, v95
	ds_read_b64_tr_b16 v[92:93], v191 offset:31744
	ds_read_b64_tr_b16 v[94:95], v191 offset:32256
	v_mfma_f32_32x32x16_bf16 v[52:67], v[172:175], v[136:139], v[52:67]
	v_add_f32_e32 v84, v98, v84
	v_add_f32_e32 v84, v99, v84
	v_add_f32_e32 v191, 0, v84
	v_cvt_pk_bf16_f32 v150, v96, v97
	v_cvt_pk_bf16_f32 v151, v98, v99
	v_lshl_add_u64 v[84:85], v[182:183], 0, s[10:11]
	s_add_i32 s27, s72, s70
	s_mov_b32 s73, m0
	s_mov_b32 m0, s27
	s_nop 0
	global_load_lds_dwordx4 v[84:85], off
	s_mov_b32 m0, s73
	v_lshl_add_u64 v[184:185], v[184:185], 0, s[4:5]
	s_add_i32 s27, s74, s69
	s_mov_b32 s73, m0
	s_mov_b32 m0, s27
	s_nop 0
	global_load_lds_dwordx4 v[184:185], off
	s_mov_b32 m0, s73
	s_waitcnt lgkmcnt(14)
	v_mfma_f32_32x32x16_bf16 v[4:19], v[160:163], v[196:199], v[4:19]
	v_exp_f32_e32 v68, v68
	v_exp_f32_e32 v69, v69
	v_exp_f32_e32 v70, v70
	v_exp_f32_e32 v71, v71
	s_waitcnt lgkmcnt(12)
	v_mfma_f32_32x32x16_bf16 v[20:35], v[160:163], v[100:103], v[20:35]
	v_exp_f32_e32 v72, v72
	v_exp_f32_e32 v73, v73
	v_exp_f32_e32 v74, v74
	v_exp_f32_e32 v75, v75
	v_add_u32_e32 v96, s74, v189
	ds_read_b128 v[84:87], v96
	ds_read_b128 v[172:175], v96 offset:512
	s_waitcnt lgkmcnt(12)
	v_mfma_f32_32x32x16_bf16 v[4:19], v[156:159], v[104:107], v[4:19]
	v_exp_f32_e32 v76, v76
	v_exp_f32_e32 v77, v77
	v_exp_f32_e32 v78, v78
	v_exp_f32_e32 v79, v79
	ds_read_b128 v[168:171], v96 offset:2048
	ds_read_b128 v[164:167], v96 offset:2560
	s_waitcnt lgkmcnt(12)
	v_mfma_f32_32x32x16_bf16 v[20:35], v[156:159], v[108:111], v[20:35]
	v_exp_f32_e32 v80, v80
	v_exp_f32_e32 v81, v81
	v_exp_f32_e32 v82, v82
	v_exp_f32_e32 v83, v83
	ds_read_b128 v[128:131], v96 offset:4096
	ds_read_b128 v[124:127], v96 offset:4608
	s_waitcnt lgkmcnt(12)
	v_mfma_f32_32x32x16_bf16 v[4:19], v[152:155], v[112:115], v[4:19]
	v_exp_f32_e32 v52, v52
	v_exp_f32_e32 v53, v53
	v_exp_f32_e32 v54, v54
	v_exp_f32_e32 v55, v55
	ds_read_b128 v[120:123], v96 offset:6144
	ds_read_b128 v[116:119], v96 offset:6656
	s_waitcnt lgkmcnt(12)
	v_mfma_f32_32x32x16_bf16 v[20:35], v[152:155], v[208:211], v[20:35]
	v_exp_f32_e32 v56, v56
	v_exp_f32_e32 v57, v57
	v_exp_f32_e32 v58, v58
	v_exp_f32_e32 v59, v59
	s_waitcnt lgkmcnt(10)
	v_mfma_f32_32x32x16_bf16 v[4:19], v[148:151], v[88:91], v[4:19]
	v_exp_f32_e32 v60, v60
	v_exp_f32_e32 v61, v61
	v_exp_f32_e32 v62, v62
	v_exp_f32_e32 v63, v63
	s_waitcnt lgkmcnt(8)
	v_mfma_f32_32x32x16_bf16 v[20:35], v[148:151], v[92:95], v[20:35]
	v_exp_f32_e32 v64, v64
	v_exp_f32_e32 v65, v65
	v_exp_f32_e32 v66, v66
	v_exp_f32_e32 v67, v67
	s_add_i32 s75, s74, 0x2000
	s_cmpk_lg_i32 s74, 0x4000
	v_add_f32_e32 v3, v3, v190
	s_mov_b32 s27, s72
	s_cselect_b32 s72, s75, 0
	s_add_i32 s71, s71, 2
	v_lshl_add_u64 v[182:183], v[182:183], 0, s[4:5]
	s_mov_b32 s73, s74
	v_add_f32_e32 v3, v3, v191
	s_cmp_gt_u32 s71, 24
	s_waitcnt vmcnt(2) lgkmcnt(0)
	s_barrier
	s_cbranch_scc0 .LBB1_24
	ds_read_b64_tr_b16 v[182:183], v188 offset:40960
	ds_read_b64_tr_b16 v[184:185], v188 offset:41472
	v_add_f32_e32 v88, v68, v69
	v_add_f32_e32 v88, v70, v88
	v_add_f32_e32 v88, v71, v88
	v_add_f32_e32 v88, v72, v88
	v_add_f32_e32 v88, v73, v88
	v_cvt_pk_bf16_f32 v160, v68, v69
	v_cvt_pk_bf16_f32 v161, v70, v71
	s_waitcnt lgkmcnt(9)
	v_mfma_f32_32x32x16_bf16 v[100:115], v[84:87], v[144:147], v[36:51]
	ds_read_b64_tr_b16 v[68:69], v188 offset:45056
	ds_read_b64_tr_b16 v[70:71], v188 offset:45568
	v_add_f32_e32 v84, v74, v88
	v_add_f32_e32 v84, v75, v84
	v_add_f32_e32 v84, v76, v84
	v_add_f32_e32 v148, v77, v84
	s_waitcnt lgkmcnt(10)
	v_mfma_f32_32x32x16_bf16 v[84:99], v[172:175], v[144:147], v[36:51]
	v_cvt_pk_bf16_f32 v162, v72, v73
	v_cvt_pk_bf16_f32 v163, v74, v75
	ds_read_b64_tr_b16 v[72:73], v188 offset:41984
	ds_read_b64_tr_b16 v[74:75], v188 offset:42496
	v_add_f32_e32 v148, v78, v148
	v_add_f32_e32 v148, v79, v148
	v_add_f32_e32 v148, v80, v148
	v_add_f32_e32 v148, v81, v148
	v_cvt_pk_bf16_f32 v156, v76, v77
	v_cvt_pk_bf16_f32 v157, v78, v79
	s_waitcnt lgkmcnt(11)
	v_mfma_f32_32x32x16_bf16 v[100:115], v[168:171], v[140:143], v[100:115]
	ds_read_b64_tr_b16 v[76:77], v188 offset:46080
	ds_read_b64_tr_b16 v[78:79], v188 offset:46592
	s_waitcnt lgkmcnt(12)
	v_mfma_f32_32x32x16_bf16 v[84:99], v[164:167], v[140:143], v[84:99]
	v_add_f32_e32 v148, v82, v148
	v_add_f32_e32 v148, v83, v148
	v_add_f32_e32 v148, v52, v148
	v_add_f32_e32 v148, v53, v148
	v_cvt_pk_bf16_f32 v158, v80, v81
	v_cvt_pk_bf16_f32 v159, v82, v83
	ds_read_b64_tr_b16 v[80:81], v188 offset:43008
	ds_read_b64_tr_b16 v[82:83], v188 offset:43520
	v_add_f32_e32 v148, v54, v148
	v_add_f32_e32 v148, v55, v148
	v_add_f32_e32 v148, v56, v148
	v_add_f32_e32 v148, v57, v148
	v_cvt_pk_bf16_f32 v152, v52, v53
	v_cvt_pk_bf16_f32 v153, v54, v55
	s_waitcnt lgkmcnt(13)
	v_mfma_f32_32x32x16_bf16 v[100:115], v[128:131], v[132:135], v[100:115]
	ds_read_b64_tr_b16 v[52:53], v188 offset:47104
	ds_read_b64_tr_b16 v[54:55], v188 offset:47616
	s_waitcnt lgkmcnt(14)
	v_mfma_f32_32x32x16_bf16 v[84:99], v[124:127], v[132:135], v[84:99]
	v_add_f32_e32 v128, v58, v148
	v_add_f32_e32 v128, v59, v128
	v_add_f32_e32 v128, v60, v128
	v_add_f32_e32 v128, v61, v128
	v_cvt_pk_bf16_f32 v154, v56, v57
	v_cvt_pk_bf16_f32 v155, v58, v59
	ds_read_b64_tr_b16 v[56:57], v188 offset:44032
	ds_read_b64_tr_b16 v[58:59], v188 offset:44544
	v_add_f32_e32 v124, v62, v128
	v_add_f32_e32 v124, v63, v124
	v_add_f32_e32 v124, v64, v124
	v_add_f32_e32 v124, v65, v124
	v_cvt_pk_bf16_f32 v148, v60, v61
	v_cvt_pk_bf16_f32 v149, v62, v63
	s_waitcnt lgkmcnt(14)
	v_mfma_f32_32x32x16_bf16 v[100:115], v[120:123], v[136:139], v[100:115]
	ds_read_b64_tr_b16 v[60:61], v188 offset:48128
	ds_read_b64_tr_b16 v[62:63], v188 offset:48640
	v_mfma_f32_32x32x16_bf16 v[84:99], v[116:119], v[136:139], v[84:99]
	v_add_f32_e32 v120, v66, v124
	v_add_f32_e32 v120, v67, v120
	v_add_f32_e32 v164, 0, v120
	v_cvt_pk_bf16_f32 v150, v64, v65
	v_cvt_pk_bf16_f32 v151, v66, v67
	s_mov_b64 s[2:3], 0x3c000
	s_cmp_lg_u32 0, -1
	v_lshl_add_u64 v[64:65], v[180:181], 0, s[2:3]
	s_mov_b32 s4, m0
	s_mov_b32 m0, s70
	s_nop 0
	global_load_lds_dwordx4 v[64:65], off
	s_mov_b32 m0, s4
	s_cselect_b32 s7, 0, 0
	s_mov_b64 s[4:5], 0x38000
	s_add_i32 s7, s7, s68
	v_lshl_add_u64 v[64:65], v[178:179], 0, s[4:5]
	s_add_i32 s6, s7, 0x8000
	s_mov_b32 s4, m0
	s_mov_b32 m0, s6
	s_nop 0
	global_load_lds_dwordx4 v[64:65], off
	s_mov_b32 m0, s4
	s_waitcnt lgkmcnt(14)
	v_mfma_f32_32x32x16_bf16 v[4:19], v[160:163], v[182:185], v[4:19]
	v_exp_f32_e32 v100, v100
	v_exp_f32_e32 v101, v101
	v_exp_f32_e32 v102, v102
	v_exp_f32_e32 v103, v103
	s_waitcnt lgkmcnt(12)
	v_mfma_f32_32x32x16_bf16 v[20:35], v[160:163], v[68:71], v[20:35]
	v_exp_f32_e32 v104, v104
	v_exp_f32_e32 v105, v105
	v_exp_f32_e32 v106, v106
	v_exp_f32_e32 v107, v107
	ds_read_b128 v[64:67], v189 offset:8192
	ds_read_b128 v[116:119], v189 offset:8704
	s_waitcnt lgkmcnt(12)
	v_mfma_f32_32x32x16_bf16 v[4:19], v[156:159], v[72:75], v[4:19]
	v_exp_f32_e32 v108, v108
	v_exp_f32_e32 v109, v109
	v_exp_f32_e32 v110, v110
	v_exp_f32_e32 v111, v111
	ds_read_b128 v[120:123], v189 offset:10240
	ds_read_b128 v[124:127], v189 offset:10752
	s_waitcnt lgkmcnt(12)
	v_mfma_f32_32x32x16_bf16 v[20:35], v[156:159], v[76:79], v[20:35]
	v_exp_f32_e32 v112, v112
	v_exp_f32_e32 v113, v113
	v_exp_f32_e32 v114, v114
	v_exp_f32_e32 v115, v115
	ds_read_b128 v[128:131], v189 offset:12288
	ds_read_b128 v[166:169], v189 offset:12800
	s_waitcnt lgkmcnt(12)
	v_mfma_f32_32x32x16_bf16 v[4:19], v[152:155], v[80:83], v[4:19]
	v_exp_f32_e32 v84, v84
	v_exp_f32_e32 v85, v85
	v_exp_f32_e32 v86, v86
	v_exp_f32_e32 v87, v87
	ds_read_b128 v[170:173], v189 offset:14336
	ds_read_b128 v[182:185], v189 offset:14848
	s_waitcnt lgkmcnt(12)
	v_mfma_f32_32x32x16_bf16 v[20:35], v[152:155], v[52:55], v[20:35]
	v_exp_f32_e32 v88, v88
	v_exp_f32_e32 v89, v89
	v_exp_f32_e32 v90, v90
	v_exp_f32_e32 v91, v91
	s_waitcnt lgkmcnt(10)
	v_mfma_f32_32x32x16_bf16 v[4:19], v[148:151], v[56:59], v[4:19]
	v_exp_f32_e32 v92, v92
	v_exp_f32_e32 v93, v93
	v_exp_f32_e32 v94, v94
	v_exp_f32_e32 v95, v95
	s_waitcnt lgkmcnt(8)
	v_mfma_f32_32x32x16_bf16 v[20:35], v[148:151], v[60:63], v[20:35]
	v_exp_f32_e32 v96, v96
	v_exp_f32_e32 v97, v97
	v_exp_f32_e32 v98, v98
	v_exp_f32_e32 v99, v99
	s_waitcnt vmcnt(2) lgkmcnt(0)
	s_barrier
	ds_read_b64_tr_b16 v[196:197], v188 offset:24576
	ds_read_b64_tr_b16 v[198:199], v188 offset:25088
	s_waitcnt lgkmcnt(9)
	v_mfma_f32_32x32x16_bf16 v[68:83], v[64:67], v[144:147], v[36:51]
	v_add_f32_e32 v52, v100, v101
	v_add_f32_e32 v52, v102, v52
	v_add_f32_e32 v52, v103, v52
	v_add_f32_e32 v52, v104, v52
	v_add_f32_e32 v52, v105, v52
	v_cvt_pk_bf16_f32 v160, v100, v101
	v_cvt_pk_bf16_f32 v161, v102, v103
	ds_read_b64_tr_b16 v[100:101], v188 offset:28672
	ds_read_b64_tr_b16 v[102:103], v188 offset:29184
	v_add_f32_e32 v52, v106, v52
	v_add_f32_e32 v52, v107, v52
	v_add_f32_e32 v52, v108, v52
	v_add_f32_e32 v148, v109, v52
	s_waitcnt lgkmcnt(10)
	v_mfma_f32_32x32x16_bf16 v[52:67], v[116:119], v[144:147], v[36:51]
	v_cvt_pk_bf16_f32 v162, v104, v105
	v_cvt_pk_bf16_f32 v163, v106, v107
	ds_read_b64_tr_b16 v[104:105], v188 offset:25600
	ds_read_b64_tr_b16 v[106:107], v188 offset:26112
	s_waitcnt lgkmcnt(11)
	v_mfma_f32_32x32x16_bf16 v[68:83], v[120:123], v[140:143], v[68:83]
	v_add_f32_e32 v116, v110, v148
	v_add_f32_e32 v116, v111, v116
	v_add_f32_e32 v116, v112, v116
	v_add_f32_e32 v116, v113, v116
	v_cvt_pk_bf16_f32 v156, v108, v109
	v_cvt_pk_bf16_f32 v157, v110, v111
	ds_read_b64_tr_b16 v[108:109], v188 offset:29696
	ds_read_b64_tr_b16 v[110:111], v188 offset:30208
	s_waitcnt lgkmcnt(12)
	v_mfma_f32_32x32x16_bf16 v[52:67], v[124:127], v[140:143], v[52:67]
	v_add_f32_e32 v116, v114, v116
	v_add_f32_e32 v116, v115, v116
	v_add_f32_e32 v116, v84, v116
	v_add_f32_e32 v116, v85, v116
	v_cvt_pk_bf16_f32 v158, v112, v113
	v_cvt_pk_bf16_f32 v159, v114, v115
	ds_read_b64_tr_b16 v[112:113], v188 offset:26624
	ds_read_b64_tr_b16 v[114:115], v188 offset:27136
	s_waitcnt lgkmcnt(13)
	v_mfma_f32_32x32x16_bf16 v[68:83], v[128:131], v[132:135], v[68:83]
	v_add_f32_e32 v116, v86, v116
	v_add_f32_e32 v116, v87, v116
	v_add_f32_e32 v116, v88, v116
	v_add_f32_e32 v116, v89, v116
	v_cvt_pk_bf16_f32 v152, v84, v85
	v_cvt_pk_bf16_f32 v153, v86, v87
	ds_read_b64_tr_b16 v[84:85], v188 offset:30720
	ds_read_b64_tr_b16 v[86:87], v188 offset:31232
	s_waitcnt lgkmcnt(14)
	v_mfma_f32_32x32x16_bf16 v[52:67], v[166:169], v[132:135], v[52:67]
	v_add_f32_e32 v116, v90, v116
	v_add_f32_e32 v116, v91, v116
	v_add_f32_e32 v116, v92, v116
	v_add_f32_e32 v116, v93, v116
	v_cvt_pk_bf16_f32 v154, v88, v89
	v_cvt_pk_bf16_f32 v155, v90, v91
	ds_read_b64_tr_b16 v[88:89], v188 offset:27648
	ds_read_b64_tr_b16 v[90:91], v188 offset:28160
	s_waitcnt lgkmcnt(14)
	v_mfma_f32_32x32x16_bf16 v[68:83], v[170:173], v[136:139], v[68:83]
	v_add_f32_e32 v116, v94, v116
	v_add_f32_e32 v116, v95, v116
	v_add_f32_e32 v116, v96, v116
	v_add_f32_e32 v116, v97, v116
	v_cvt_pk_bf16_f32 v148, v92, v93
	v_cvt_pk_bf16_f32 v149, v94, v95
	ds_read_b64_tr_b16 v[92:93], v188 offset:31744
	ds_read_b64_tr_b16 v[94:95], v188 offset:32256
	v_mfma_f32_32x32x16_bf16 v[52:67], v[182:185], v[136:139], v[52:67]
	v_add_f32_e32 v116, v98, v116
	v_add_f32_e32 v116, v99, v116
	v_add_f32_e32 v165, 0, v116
	v_cvt_pk_bf16_f32 v150, v96, v97
	v_cvt_pk_bf16_f32 v151, v98, v99
	s_mov_b64 s[4:5], 0x3e000
	v_lshl_add_u64 v[96:97], v[180:181], 0, s[4:5]
	s_add_i32 s10, s7, 0x2000
	s_mov_b32 s11, m0
	s_mov_b32 m0, s10
	s_nop 0
	global_load_lds_dwordx4 v[96:97], off
	s_mov_b32 m0, s11
	s_mov_b64 s[10:11], 0x3a000
	v_lshl_add_u64 v[96:97], v[178:179], 0, s[10:11]
	s_add_i32 s7, s7, 0xa000
	s_mov_b32 s10, m0
	s_mov_b32 m0, s7
	s_nop 0
	global_load_lds_dwordx4 v[96:97], off
	s_mov_b32 m0, s10
	s_waitcnt lgkmcnt(14)
	v_mfma_f32_32x32x16_bf16 v[4:19], v[160:163], v[196:199], v[4:19]
	v_exp_f32_e32 v68, v68
	v_exp_f32_e32 v69, v69
	v_exp_f32_e32 v70, v70
	v_exp_f32_e32 v71, v71
	s_waitcnt lgkmcnt(12)
	v_mfma_f32_32x32x16_bf16 v[20:35], v[160:163], v[100:103], v[20:35]
	v_exp_f32_e32 v72, v72
	v_exp_f32_e32 v73, v73
	v_exp_f32_e32 v74, v74
	v_exp_f32_e32 v75, v75
	ds_read_b128 v[96:99], v189 offset:16384
	ds_read_b128 v[100:103], v189 offset:16896
	s_waitcnt lgkmcnt(12)
	v_mfma_f32_32x32x16_bf16 v[4:19], v[156:159], v[104:107], v[4:19]
	v_exp_f32_e32 v76, v76
	v_exp_f32_e32 v77, v77
	v_exp_f32_e32 v78, v78
	v_exp_f32_e32 v79, v79
	ds_read_b128 v[104:107], v189 offset:18432
	ds_read_b128 v[166:169], v189 offset:18944
	s_waitcnt lgkmcnt(12)
	v_mfma_f32_32x32x16_bf16 v[20:35], v[156:159], v[108:111], v[20:35]
	v_exp_f32_e32 v80, v80
	v_exp_f32_e32 v81, v81
	v_exp_f32_e32 v82, v82
	v_exp_f32_e32 v83, v83
	ds_read_b128 v[108:111], v189 offset:20480
	ds_read_b128 v[170:173], v189 offset:20992
	s_waitcnt lgkmcnt(12)
	v_mfma_f32_32x32x16_bf16 v[4:19], v[152:155], v[112:115], v[4:19]
	v_exp_f32_e32 v52, v52
	v_exp_f32_e32 v53, v53
	v_exp_f32_e32 v54, v54
	v_exp_f32_e32 v55, v55
	ds_read_b128 v[112:115], v189 offset:22528
	ds_read_b128 v[180:183], v189 offset:23040
	s_waitcnt lgkmcnt(12)
	v_mfma_f32_32x32x16_bf16 v[20:35], v[152:155], v[84:87], v[20:35]
	v_exp_f32_e32 v56, v56
	v_exp_f32_e32 v57, v57
	v_exp_f32_e32 v58, v58
	v_exp_f32_e32 v59, v59
	s_waitcnt lgkmcnt(10)
	v_mfma_f32_32x32x16_bf16 v[4:19], v[148:151], v[88:91], v[4:19]
	v_exp_f32_e32 v60, v60
	v_exp_f32_e32 v61, v61
	v_exp_f32_e32 v62, v62
	v_exp_f32_e32 v63, v63
	s_waitcnt lgkmcnt(8)
	v_mfma_f32_32x32x16_bf16 v[20:35], v[148:151], v[92:95], v[20:35]
	v_exp_f32_e32 v64, v64
	v_exp_f32_e32 v65, v65
	v_exp_f32_e32 v66, v66
	v_exp_f32_e32 v67, v67
	s_waitcnt vmcnt(2) lgkmcnt(0)
	s_barrier
	ds_read_b64_tr_b16 v[196:197], v188 offset:32768
	ds_read_b64_tr_b16 v[198:199], v188 offset:33280
	v_add_f32_e32 v84, v68, v69
	v_add_f32_e32 v84, v70, v84
	v_add_f32_e32 v84, v71, v84
	v_add_f32_e32 v84, v72, v84
	v_add_f32_e32 v84, v73, v84
	v_cvt_pk_bf16_f32 v160, v68, v69
	v_cvt_pk_bf16_f32 v161, v70, v71
	s_waitcnt lgkmcnt(9)
	v_mfma_f32_32x32x16_bf16 v[116:131], v[96:99], v[144:147], v[36:51]
	ds_read_b64_tr_b16 v[68:69], v188 offset:36864
	ds_read_b64_tr_b16 v[70:71], v188 offset:37376
	v_add_f32_e32 v84, v74, v84
	v_add_f32_e32 v84, v75, v84
	v_add_f32_e32 v84, v76, v84
	v_add_f32_e32 v148, v77, v84
	s_waitcnt lgkmcnt(10)
	v_mfma_f32_32x32x16_bf16 v[84:99], v[100:103], v[144:147], v[36:51]
	v_cvt_pk_bf16_f32 v162, v72, v73
	v_cvt_pk_bf16_f32 v163, v74, v75
	ds_read_b64_tr_b16 v[72:73], v188 offset:33792
	ds_read_b64_tr_b16 v[74:75], v188 offset:34304
	v_add_f32_e32 v100, v78, v148
	v_add_f32_e32 v100, v79, v100
	v_add_f32_e32 v100, v80, v100
	v_add_f32_e32 v100, v81, v100
	v_cvt_pk_bf16_f32 v156, v76, v77
	v_cvt_pk_bf16_f32 v157, v78, v79
	s_waitcnt lgkmcnt(11)
	v_mfma_f32_32x32x16_bf16 v[116:131], v[104:107], v[140:143], v[116:131]
	ds_read_b64_tr_b16 v[76:77], v188 offset:37888
	ds_read_b64_tr_b16 v[78:79], v188 offset:38400
	s_waitcnt lgkmcnt(12)
	v_mfma_f32_32x32x16_bf16 v[84:99], v[166:169], v[140:143], v[84:99]
	v_add_f32_e32 v100, v82, v100
	v_add_f32_e32 v100, v83, v100
	v_add_f32_e32 v100, v52, v100
	v_add_f32_e32 v100, v53, v100
	v_cvt_pk_bf16_f32 v158, v80, v81
	v_cvt_pk_bf16_f32 v159, v82, v83
	ds_read_b64_tr_b16 v[80:81], v188 offset:34816
	ds_read_b64_tr_b16 v[82:83], v188 offset:35328
	v_add_f32_e32 v100, v54, v100
	v_add_f32_e32 v100, v55, v100
	v_add_f32_e32 v100, v56, v100
	v_add_f32_e32 v100, v57, v100
	v_cvt_pk_bf16_f32 v152, v52, v53
	v_cvt_pk_bf16_f32 v153, v54, v55
	s_waitcnt lgkmcnt(13)
	v_mfma_f32_32x32x16_bf16 v[116:131], v[108:111], v[132:135], v[116:131]
	ds_read_b64_tr_b16 v[52:53], v188 offset:38912
	ds_read_b64_tr_b16 v[54:55], v188 offset:39424
	s_waitcnt lgkmcnt(14)
	v_mfma_f32_32x32x16_bf16 v[84:99], v[170:173], v[132:135], v[84:99]
	v_add_f32_e32 v100, v58, v100
	v_add_f32_e32 v100, v59, v100
	v_add_f32_e32 v100, v60, v100
	v_add_f32_e32 v100, v61, v100
	v_cvt_pk_bf16_f32 v154, v56, v57
	v_cvt_pk_bf16_f32 v155, v58, v59
	ds_read_b64_tr_b16 v[56:57], v188 offset:35840
	ds_read_b64_tr_b16 v[58:59], v188 offset:36352
	v_add_f32_e32 v100, v62, v100
	v_add_f32_e32 v100, v63, v100
	v_add_f32_e32 v100, v64, v100
	v_add_f32_e32 v100, v65, v100
	v_cvt_pk_bf16_f32 v148, v60, v61
	v_cvt_pk_bf16_f32 v149, v62, v63
	s_waitcnt lgkmcnt(14)
	v_mfma_f32_32x32x16_bf16 v[116:131], v[112:115], v[136:139], v[116:131]
	ds_read_b64_tr_b16 v[60:61], v188 offset:39936
	ds_read_b64_tr_b16 v[62:63], v188 offset:40448
	v_mfma_f32_32x32x16_bf16 v[84:99], v[180:183], v[136:139], v[84:99]
	v_add_f32_e32 v100, v66, v100
	v_add_f32_e32 v100, v67, v100
	v_add_f32_e32 v166, 0, v100
	v_cvt_pk_bf16_f32 v150, v64, v65
	v_cvt_pk_bf16_f32 v151, v66, v67
	v_lshl_add_u64 v[64:65], v[178:179], 0, s[2:3]
	s_mov_b32 s2, m0
	s_mov_b32 m0, s69
	s_nop 0
	global_load_lds_dwordx4 v[64:65], off
	s_mov_b32 m0, s2
	s_waitcnt lgkmcnt(14)
	v_mfma_f32_32x32x16_bf16 v[4:19], v[160:163], v[196:199], v[4:19]
	s_nop 0
	v_exp_f32_e32 v116, v116
	v_exp_f32_e32 v117, v117
	v_exp_f32_e32 v118, v118
	v_exp_f32_e32 v119, v119
	s_waitcnt lgkmcnt(12)
	v_mfma_f32_32x32x16_bf16 v[20:35], v[160:163], v[68:71], v[20:35]
	v_exp_f32_e32 v120, v120
	v_exp_f32_e32 v121, v121
	v_exp_f32_e32 v122, v122
	v_exp_f32_e32 v123, v123
	ds_read_b128 v[64:67], v189
	ds_read_b128 v[168:171], v189 offset:512
	s_waitcnt lgkmcnt(12)
	v_mfma_f32_32x32x16_bf16 v[4:19], v[156:159], v[72:75], v[4:19]
	v_exp_f32_e32 v124, v124
	v_exp_f32_e32 v125, v125
	v_exp_f32_e32 v126, v126
	v_exp_f32_e32 v127, v127
	ds_read_b128 v[172:175], v189 offset:2048
	ds_read_b128 v[180:183], v189 offset:2560
	s_waitcnt lgkmcnt(12)
	v_mfma_f32_32x32x16_bf16 v[20:35], v[156:159], v[76:79], v[20:35]
	v_exp_f32_e32 v128, v128
	v_exp_f32_e32 v129, v129
	v_exp_f32_e32 v130, v130
	v_exp_f32_e32 v131, v131
	ds_read_b128 v[196:199], v189 offset:4096
	ds_read_b128 v[208:211], v189 offset:4608
	s_waitcnt lgkmcnt(12)
	v_mfma_f32_32x32x16_bf16 v[4:19], v[152:155], v[80:83], v[4:19]
	v_exp_f32_e32 v84, v84
	v_exp_f32_e32 v85, v85
	v_exp_f32_e32 v86, v86
	v_exp_f32_e32 v87, v87
	ds_read_b128 v[212:215], v189 offset:6144
	ds_read_b128 v[216:219], v189 offset:6656
	s_waitcnt lgkmcnt(12)
	v_mfma_f32_32x32x16_bf16 v[20:35], v[152:155], v[52:55], v[20:35]
	v_exp_f32_e32 v88, v88
	v_exp_f32_e32 v89, v89
	v_exp_f32_e32 v90, v90
	v_exp_f32_e32 v91, v91
	s_waitcnt lgkmcnt(10)
	v_mfma_f32_32x32x16_bf16 v[4:19], v[148:151], v[56:59], v[4:19]
	v_exp_f32_e32 v92, v92
	v_exp_f32_e32 v93, v93
	v_exp_f32_e32 v94, v94
	v_exp_f32_e32 v95, v95
	s_waitcnt lgkmcnt(8)
	v_mfma_f32_32x32x16_bf16 v[20:35], v[148:151], v[60:63], v[20:35]
	v_exp_f32_e32 v96, v96
	v_exp_f32_e32 v97, v97
	v_exp_f32_e32 v98, v98
	v_exp_f32_e32 v99, v99
	s_waitcnt vmcnt(1) lgkmcnt(0)
	s_barrier
	ds_read_b64_tr_b16 v[52:53], v188 offset:40960
	ds_read_b64_tr_b16 v[54:55], v188 offset:41472
	v_add_f32_e32 v56, v116, v117
	v_add_f32_e32 v56, v118, v56
	v_add_f32_e32 v56, v119, v56
	v_add_f32_e32 v56, v120, v56
	v_add_f32_e32 v60, v121, v56
	v_cvt_pk_bf16_f32 v160, v116, v117
	v_cvt_pk_bf16_f32 v161, v118, v119
	s_waitcnt lgkmcnt(9)
	v_mfma_f32_32x32x16_bf16 v[100:115], v[64:67], v[144:147], v[36:51]
	ds_read_b64_tr_b16 v[56:57], v188 offset:45056
	ds_read_b64_tr_b16 v[58:59], v188 offset:45568
	s_waitcnt lgkmcnt(10)
	v_mfma_f32_32x32x16_bf16 v[68:83], v[168:171], v[144:147], v[36:51]
	v_add_f32_e32 v60, v122, v60
	v_add_f32_e32 v60, v123, v60
	v_add_f32_e32 v60, v124, v60
	v_add_f32_e32 v64, v125, v60
	v_cvt_pk_bf16_f32 v162, v120, v121
	v_cvt_pk_bf16_f32 v163, v122, v123
	ds_read_b64_tr_b16 v[60:61], v188 offset:41984
	ds_read_b64_tr_b16 v[62:63], v188 offset:42496
	v_add_f32_e32 v64, v126, v64
	v_add_f32_e32 v64, v127, v64
	v_add_f32_e32 v64, v128, v64
	v_add_f32_e32 v116, v129, v64
	v_cvt_pk_bf16_f32 v156, v124, v125
	v_cvt_pk_bf16_f32 v157, v126, v127
	s_waitcnt lgkmcnt(11)
	v_mfma_f32_32x32x16_bf16 v[100:115], v[172:175], v[140:143], v[100:115]
	ds_read_b64_tr_b16 v[64:65], v188 offset:46080
	ds_read_b64_tr_b16 v[66:67], v188 offset:46592
	s_waitcnt lgkmcnt(12)
	v_mfma_f32_32x32x16_bf16 v[68:83], v[180:183], v[140:143], v[68:83]
	v_add_f32_e32 v116, v130, v116
	v_add_f32_e32 v116, v131, v116
	v_add_f32_e32 v116, v84, v116
	v_add_f32_e32 v120, v85, v116
	v_cvt_pk_bf16_f32 v158, v128, v129
	v_cvt_pk_bf16_f32 v159, v130, v131
	ds_read_b64_tr_b16 v[116:117], v188 offset:43008
	ds_read_b64_tr_b16 v[118:119], v188 offset:43520
	v_add_f32_e32 v120, v86, v120
	v_add_f32_e32 v120, v87, v120
	v_add_f32_e32 v120, v88, v120
	v_add_f32_e32 v124, v89, v120
	v_cvt_pk_bf16_f32 v152, v84, v85
	v_cvt_pk_bf16_f32 v153, v86, v87
	s_waitcnt lgkmcnt(13)
	v_mfma_f32_32x32x16_bf16 v[100:115], v[196:199], v[132:135], v[100:115]
	ds_read_b64_tr_b16 v[120:121], v188 offset:47104
	ds_read_b64_tr_b16 v[122:123], v188 offset:47616
	s_waitcnt lgkmcnt(14)
	v_mfma_f32_32x32x16_bf16 v[68:83], v[208:211], v[132:135], v[68:83]
	v_add_f32_e32 v84, v90, v124
	v_add_f32_e32 v84, v91, v84
	v_add_f32_e32 v84, v92, v84
	v_add_f32_e32 v84, v93, v84
	v_cvt_pk_bf16_f32 v154, v88, v89
	v_cvt_pk_bf16_f32 v155, v90, v91
	ds_read_b64_tr_b16 v[86:87], v188 offset:44032
	ds_read_b64_tr_b16 v[88:89], v188 offset:44544
	v_add_f32_e32 v84, v94, v84
	v_add_f32_e32 v84, v95, v84
	v_add_f32_e32 v84, v96, v84
	v_add_f32_e32 v84, v97, v84
	v_cvt_pk_bf16_f32 v148, v92, v93
	v_cvt_pk_bf16_f32 v149, v94, v95
	s_waitcnt lgkmcnt(14)
	v_mfma_f32_32x32x16_bf16 v[100:115], v[212:215], v[136:139], v[100:115]
	ds_read_b64_tr_b16 v[90:91], v188 offset:48128
	ds_read_b64_tr_b16 v[92:93], v188 offset:48640
	v_mfma_f32_32x32x16_bf16 v[68:83], v[216:219], v[136:139], v[68:83]
	v_add_f32_e32 v84, v98, v84
	v_add_f32_e32 v84, v99, v84
	v_add_f32_e32 v84, 0, v84
	v_cvt_pk_bf16_f32 v150, v96, v97
	v_cvt_pk_bf16_f32 v151, v98, v99
	v_lshl_add_u64 v[94:95], v[178:179], 0, s[4:5]
	s_mov_b32 s2, m0
	s_mov_b32 m0, s6
	s_nop 0
	global_load_lds_dwordx4 v[94:95], off
	s_mov_b32 m0, s2
	s_waitcnt lgkmcnt(14)
	v_mfma_f32_32x32x16_bf16 v[4:19], v[160:163], v[52:55], v[4:19]
	s_nop 0
	v_exp_f32_e32 v100, v100
	v_exp_f32_e32 v101, v101
	v_exp_f32_e32 v102, v102
	v_exp_f32_e32 v103, v103
	s_waitcnt lgkmcnt(12)
	v_mfma_f32_32x32x16_bf16 v[20:35], v[160:163], v[56:59], v[20:35]
	v_exp_f32_e32 v104, v104
	v_exp_f32_e32 v105, v105
	v_exp_f32_e32 v106, v106
	v_exp_f32_e32 v107, v107
	ds_read_b128 v[94:97], v189 offset:8192
	ds_read_b128 v[124:127], v189 offset:8704
	s_waitcnt lgkmcnt(12)
	v_mfma_f32_32x32x16_bf16 v[4:19], v[156:159], v[60:63], v[4:19]
	v_exp_f32_e32 v108, v108
	v_exp_f32_e32 v109, v109
	v_exp_f32_e32 v110, v110
	v_exp_f32_e32 v111, v111
	ds_read_b128 v[128:131], v189 offset:10240
	ds_read_b128 v[168:171], v189 offset:10752
	s_waitcnt lgkmcnt(12)
	v_mfma_f32_32x32x16_bf16 v[20:35], v[156:159], v[64:67], v[20:35]
	v_exp_f32_e32 v112, v112
	v_exp_f32_e32 v113, v113
	v_exp_f32_e32 v114, v114
	v_exp_f32_e32 v115, v115
	ds_read_b128 v[172:175], v189 offset:12288
	ds_read_b128 v[178:181], v189 offset:12800
	s_waitcnt lgkmcnt(12)
	v_mfma_f32_32x32x16_bf16 v[4:19], v[152:155], v[116:119], v[4:19]
	v_exp_f32_e32 v68, v68
	v_exp_f32_e32 v69, v69
	v_exp_f32_e32 v70, v70
	v_exp_f32_e32 v71, v71
	ds_read_b128 v[116:119], v189 offset:14336
	ds_read_b128 v[182:185], v189 offset:14848
	s_waitcnt lgkmcnt(12)
	v_mfma_f32_32x32x16_bf16 v[20:35], v[152:155], v[120:123], v[20:35]
	v_exp_f32_e32 v72, v72
	v_exp_f32_e32 v73, v73
	v_exp_f32_e32 v74, v74
	v_exp_f32_e32 v75, v75
	s_waitcnt lgkmcnt(10)
	v_mfma_f32_32x32x16_bf16 v[4:19], v[148:151], v[86:89], v[4:19]
	v_exp_f32_e32 v76, v76
	v_exp_f32_e32 v77, v77
	v_exp_f32_e32 v78, v78
	v_exp_f32_e32 v79, v79
	s_waitcnt lgkmcnt(8)
	v_mfma_f32_32x32x16_bf16 v[20:35], v[148:151], v[90:93], v[20:35]
	v_exp_f32_e32 v80, v80
	v_exp_f32_e32 v81, v81
	v_exp_f32_e32 v82, v82
	v_exp_f32_e32 v83, v83
	s_waitcnt vmcnt(0) lgkmcnt(0)
	s_barrier
	ds_read_b64_tr_b16 v[86:87], v188 offset:24576
	ds_read_b64_tr_b16 v[88:89], v188 offset:25088
	v_add_f32_e32 v52, v100, v101
	v_add_f32_e32 v52, v102, v52
	v_add_f32_e32 v52, v103, v52
	v_add_f32_e32 v52, v104, v52
	v_add_f32_e32 v85, v105, v52
	s_waitcnt lgkmcnt(9)
	v_mfma_f32_32x32x16_bf16 v[52:67], v[94:97], v[144:147], v[36:51]
	v_cvt_pk_bf16_f32 v160, v100, v101
	v_cvt_pk_bf16_f32 v161, v102, v103
	ds_read_b64_tr_b16 v[90:91], v188 offset:28672
	ds_read_b64_tr_b16 v[92:93], v188 offset:29184
	s_waitcnt lgkmcnt(10)
	v_mfma_f32_32x32x16_bf16 v[36:51], v[124:127], v[144:147], v[36:51]
	v_add_f32_e32 v85, v106, v85
	v_add_f32_e32 v85, v107, v85
	v_add_f32_e32 v85, v108, v85
	v_add_f32_e32 v85, v109, v85
	v_cvt_pk_bf16_f32 v162, v104, v105
	v_cvt_pk_bf16_f32 v163, v106, v107
	ds_read_b64_tr_b16 v[94:95], v188 offset:25600
	ds_read_b64_tr_b16 v[96:97], v188 offset:26112
	s_waitcnt lgkmcnt(11)
	v_mfma_f32_32x32x16_bf16 v[52:67], v[128:131], v[140:143], v[52:67]
	v_add_f32_e32 v85, v110, v85
	v_add_f32_e32 v85, v111, v85
	v_add_f32_e32 v85, v112, v85
	v_add_f32_e32 v85, v113, v85
	v_cvt_pk_bf16_f32 v156, v108, v109
	v_cvt_pk_bf16_f32 v157, v110, v111
	ds_read_b64_tr_b16 v[98:99], v188 offset:29696
	ds_read_b64_tr_b16 v[100:101], v188 offset:30208
	s_waitcnt lgkmcnt(12)
	v_mfma_f32_32x32x16_bf16 v[36:51], v[168:171], v[140:143], v[36:51]
	v_add_f32_e32 v85, v114, v85
	v_add_f32_e32 v85, v115, v85
	v_add_f32_e32 v85, v68, v85
	v_add_f32_e32 v85, v69, v85
	v_cvt_pk_bf16_f32 v158, v112, v113
	v_cvt_pk_bf16_f32 v159, v114, v115
	ds_read_b64_tr_b16 v[102:103], v188 offset:26624
	ds_read_b64_tr_b16 v[104:105], v188 offset:27136
	s_waitcnt lgkmcnt(13)
	v_mfma_f32_32x32x16_bf16 v[52:67], v[172:175], v[132:135], v[52:67]
	v_add_f32_e32 v85, v70, v85
	v_add_f32_e32 v85, v71, v85
	v_add_f32_e32 v85, v72, v85
	v_add_f32_e32 v85, v73, v85
	v_cvt_pk_bf16_f32 v152, v68, v69
	v_cvt_pk_bf16_f32 v153, v70, v71
	ds_read_b64_tr_b16 v[106:107], v188 offset:30720
	ds_read_b64_tr_b16 v[108:109], v188 offset:31232
	s_waitcnt lgkmcnt(14)
	v_mfma_f32_32x32x16_bf16 v[36:51], v[178:181], v[132:135], v[36:51]
	v_add_f32_e32 v68, v74, v85
	v_add_f32_e32 v68, v75, v68
	v_add_f32_e32 v68, v76, v68
	v_add_f32_e32 v68, v77, v68
	v_cvt_pk_bf16_f32 v154, v72, v73
	v_cvt_pk_bf16_f32 v155, v74, v75
	ds_read_b64_tr_b16 v[70:71], v188 offset:27648
	ds_read_b64_tr_b16 v[72:73], v188 offset:28160
	s_waitcnt lgkmcnt(14)
	v_mfma_f32_32x32x16_bf16 v[52:67], v[116:119], v[136:139], v[52:67]
	v_add_f32_e32 v68, v78, v68
	v_add_f32_e32 v68, v79, v68
	v_add_f32_e32 v68, v80, v68
	v_add_f32_e32 v68, v81, v68
	v_cvt_pk_bf16_f32 v148, v76, v77
	v_cvt_pk_bf16_f32 v149, v78, v79
	ds_read_b64_tr_b16 v[74:75], v188 offset:31744
	ds_read_b64_tr_b16 v[76:77], v188 offset:32256
	v_mfma_f32_32x32x16_bf16 v[36:51], v[182:185], v[136:139], v[36:51]
	v_add_f32_e32 v68, v82, v68
	v_add_f32_e32 v68, v83, v68
	v_add_f32_e32 v68, 0, v68
	v_cvt_pk_bf16_f32 v150, v80, v81
	v_cvt_pk_bf16_f32 v151, v82, v83
	s_waitcnt lgkmcnt(14)
	v_mfma_f32_32x32x16_bf16 v[4:19], v[160:163], v[86:89], v[4:19]
	v_exp_f32_e32 v52, v52
	v_exp_f32_e32 v53, v53
	v_exp_f32_e32 v54, v54
	v_exp_f32_e32 v55, v55
	s_waitcnt lgkmcnt(12)
	v_mfma_f32_32x32x16_bf16 v[20:35], v[160:163], v[90:93], v[20:35]
	v_exp_f32_e32 v56, v56
	v_exp_f32_e32 v57, v57
	v_exp_f32_e32 v58, v58
	v_exp_f32_e32 v59, v59
	s_waitcnt lgkmcnt(10)
	v_mfma_f32_32x32x16_bf16 v[4:19], v[156:159], v[94:97], v[4:19]
	v_exp_f32_e32 v60, v60
	v_exp_f32_e32 v61, v61
	v_exp_f32_e32 v62, v62
	v_exp_f32_e32 v63, v63
	s_waitcnt lgkmcnt(8)
	v_mfma_f32_32x32x16_bf16 v[20:35], v[156:159], v[98:101], v[20:35]
	v_exp_f32_e32 v64, v64
	v_exp_f32_e32 v65, v65
	v_exp_f32_e32 v66, v66
	v_exp_f32_e32 v67, v67
	s_waitcnt lgkmcnt(6)
	v_mfma_f32_32x32x16_bf16 v[4:19], v[152:155], v[102:105], v[4:19]
	v_exp_f32_e32 v36, v36
	v_exp_f32_e32 v37, v37
	v_exp_f32_e32 v38, v38
	v_exp_f32_e32 v39, v39
	s_waitcnt lgkmcnt(4)
	v_mfma_f32_32x32x16_bf16 v[20:35], v[152:155], v[106:109], v[20:35]
	v_exp_f32_e32 v40, v40
	v_exp_f32_e32 v41, v41
	v_exp_f32_e32 v42, v42
	v_exp_f32_e32 v43, v43
	s_waitcnt lgkmcnt(2)
	v_mfma_f32_32x32x16_bf16 v[4:19], v[148:151], v[70:73], v[4:19]
	v_exp_f32_e32 v44, v44
	v_exp_f32_e32 v45, v45
	v_exp_f32_e32 v46, v46
	v_exp_f32_e32 v47, v47
	s_waitcnt lgkmcnt(0)
	v_mfma_f32_32x32x16_bf16 v[20:35], v[148:151], v[74:77], v[20:35]
	v_exp_f32_e32 v48, v48
	v_exp_f32_e32 v49, v49
	v_exp_f32_e32 v50, v50
	v_exp_f32_e32 v51, v51
	s_and_b64 vcc, exec, s[24:25]
	s_cbranch_vccz .LBB1_32
	s_cmp_lg_u64 s[22:23], 0
	s_cselect_b64 s[2:3], -1, 0
	v_cmp_eq_u32_e32 vcc, 0, v0
	s_and_b64 s[4:5], vcc, s[2:3]
	s_and_saveexec_b64 s[2:3], s[4:5]
	s_cbranch_execz .LBB1_31
	v_mov_b32_e32 v69, 0
	global_load_dword v70, v69, s[22:23] sc1
	s_movk_i32 s4, 0x7f
	s_waitcnt vmcnt(0)
	v_cmp_lt_u32_e32 vcc, s4, v70
	s_cbranch_vccnz .LBB1_30
	s_mov_b32 s5, 0
	s_movk_i32 s4, 0x80

.LBB1_142:
	v_add_u32_e32 v189, s9, v187
	ds_read_b64_tr_b16 v[190:191], v189 offset:24576
	ds_read_b64_tr_b16 v[192:193], v189 offset:25088
	v_add_f32_e32 v88, v68, v69
	v_add_f32_e32 v88, v70, v88
	v_add_f32_e32 v88, v71, v88
	v_add_f32_e32 v88, v72, v88
	v_add_f32_e32 v88, v73, v88
	v_cvt_pk_bf16_f32 v160, v68, v69
	v_cvt_pk_bf16_f32 v161, v70, v71
	s_waitcnt lgkmcnt(9)
	v_mfma_f32_32x32x16_bf16 v[100:115], v[84:87], v[144:147], v[36:51]
	ds_read_b64_tr_b16 v[68:69], v189 offset:28672
	ds_read_b64_tr_b16 v[70:71], v189 offset:29184
	v_add_f32_e32 v84, v74, v88
	v_add_f32_e32 v84, v75, v84
	v_add_f32_e32 v84, v76, v84
	v_add_f32_e32 v148, v77, v84
	s_waitcnt lgkmcnt(10)
	v_mfma_f32_32x32x16_bf16 v[84:99], v[172:175], v[144:147], v[36:51]
	v_cvt_pk_bf16_f32 v162, v72, v73
	v_cvt_pk_bf16_f32 v163, v74, v75
	ds_read_b64_tr_b16 v[72:73], v189 offset:25600
	ds_read_b64_tr_b16 v[74:75], v189 offset:26112
	v_add_f32_e32 v148, v78, v148
	v_add_f32_e32 v148, v79, v148
	v_add_f32_e32 v148, v80, v148
	v_add_f32_e32 v148, v81, v148
	v_cvt_pk_bf16_f32 v156, v76, v77
	v_cvt_pk_bf16_f32 v157, v78, v79
	s_waitcnt lgkmcnt(11)
	v_mfma_f32_32x32x16_bf16 v[100:115], v[168:171], v[140:143], v[100:115]
	ds_read_b64_tr_b16 v[76:77], v189 offset:29696
	ds_read_b64_tr_b16 v[78:79], v189 offset:30208
	s_waitcnt lgkmcnt(12)
	v_mfma_f32_32x32x16_bf16 v[84:99], v[164:167], v[140:143], v[84:99]
	v_add_f32_e32 v148, v82, v148
	v_add_f32_e32 v148, v83, v148
	v_add_f32_e32 v148, v52, v148
	v_add_f32_e32 v148, v53, v148
	v_cvt_pk_bf16_f32 v158, v80, v81
	v_cvt_pk_bf16_f32 v159, v82, v83
	ds_read_b64_tr_b16 v[80:81], v189 offset:26624
	ds_read_b64_tr_b16 v[82:83], v189 offset:27136
	v_add_f32_e32 v148, v54, v148
	v_add_f32_e32 v148, v55, v148
	v_add_f32_e32 v148, v56, v148
	v_add_f32_e32 v148, v57, v148
	v_cvt_pk_bf16_f32 v152, v52, v53
	v_cvt_pk_bf16_f32 v153, v54, v55
	s_waitcnt lgkmcnt(13)
	v_mfma_f32_32x32x16_bf16 v[100:115], v[128:131], v[132:135], v[100:115]
	ds_read_b64_tr_b16 v[52:53], v189 offset:30720
	ds_read_b64_tr_b16 v[54:55], v189 offset:31232
	s_waitcnt lgkmcnt(14)
	v_mfma_f32_32x32x16_bf16 v[84:99], v[124:127], v[132:135], v[84:99]
	v_add_f32_e32 v128, v58, v148
	v_add_f32_e32 v128, v59, v128
	v_add_f32_e32 v128, v60, v128
	v_add_f32_e32 v128, v61, v128
	v_cvt_pk_bf16_f32 v154, v56, v57
	v_cvt_pk_bf16_f32 v155, v58, v59
	ds_read_b64_tr_b16 v[56:57], v189 offset:27648
	ds_read_b64_tr_b16 v[58:59], v189 offset:28160
	v_add_f32_e32 v124, v62, v128
	v_add_f32_e32 v124, v63, v124
	v_add_f32_e32 v124, v64, v124
	v_add_f32_e32 v124, v65, v124
	v_cvt_pk_bf16_f32 v148, v60, v61
	v_cvt_pk_bf16_f32 v149, v62, v63
	s_waitcnt lgkmcnt(14)
	v_mfma_f32_32x32x16_bf16 v[100:115], v[120:123], v[136:139], v[100:115]
	ds_read_b64_tr_b16 v[60:61], v189 offset:31744
	ds_read_b64_tr_b16 v[62:63], v189 offset:32256
	v_mfma_f32_32x32x16_bf16 v[84:99], v[116:119], v[136:139], v[84:99]
	v_add_f32_e32 v120, v66, v124
	v_add_f32_e32 v120, v67, v120
	v_add_f32_e32 v189, 0, v120
	v_cvt_pk_bf16_f32 v150, v64, v65
	v_cvt_pk_bf16_f32 v151, v66, v67
	v_lshl_add_u64 v[64:65], v[180:181], 0, s[0:1]
	s_add_i32 s9, s29, s20
	s_mov_b32 s30, m0
	s_mov_b32 m0, s9
	s_nop 0
	global_load_lds_dwordx4 v[64:65], off
	s_mov_b32 m0, s30
	v_lshl_add_u64 v[64:65], v[182:183], 0, s[2:3]
	s_add_i32 s9, s28, s8
	s_mov_b32 s30, m0
	s_mov_b32 m0, s9
	s_nop 0
	global_load_lds_dwordx4 v[64:65], off
	s_mov_b32 m0, s30
	s_waitcnt lgkmcnt(14)
	v_mfma_f32_32x32x16_bf16 v[4:19], v[160:163], v[190:193], v[4:19]
	v_exp_f32_e32 v100, v100
	v_exp_f32_e32 v101, v101
	v_exp_f32_e32 v102, v102
	v_exp_f32_e32 v103, v103
	s_waitcnt lgkmcnt(12)
	v_mfma_f32_32x32x16_bf16 v[20:35], v[160:163], v[68:71], v[20:35]
	v_exp_f32_e32 v104, v104
	v_exp_f32_e32 v105, v105
	v_exp_f32_e32 v106, v106
	v_exp_f32_e32 v107, v107
	v_add_u32_e32 v68, s28, v188
	ds_read_b128 v[64:67], v68
	ds_read_b128 v[116:119], v68 offset:512
	s_waitcnt lgkmcnt(12)
	v_mfma_f32_32x32x16_bf16 v[4:19], v[156:159], v[72:75], v[4:19]
	v_exp_f32_e32 v108, v108
	v_exp_f32_e32 v109, v109
	v_exp_f32_e32 v110, v110
	v_exp_f32_e32 v111, v111
	ds_read_b128 v[120:123], v68 offset:2048
	ds_read_b128 v[124:127], v68 offset:2560
	s_waitcnt lgkmcnt(12)
	v_mfma_f32_32x32x16_bf16 v[20:35], v[156:159], v[76:79], v[20:35]
	v_exp_f32_e32 v112, v112
	v_exp_f32_e32 v113, v113
	v_exp_f32_e32 v114, v114
	v_exp_f32_e32 v115, v115
	ds_read_b128 v[128:131], v68 offset:4096
	ds_read_b128 v[164:167], v68 offset:4608
	s_waitcnt lgkmcnt(12)
	v_mfma_f32_32x32x16_bf16 v[4:19], v[152:155], v[80:83], v[4:19]
	v_exp_f32_e32 v84, v84
	v_exp_f32_e32 v85, v85
	v_exp_f32_e32 v86, v86
	v_exp_f32_e32 v87, v87
	ds_read_b128 v[168:171], v68 offset:6144
	ds_read_b128 v[172:175], v68 offset:6656
	s_waitcnt lgkmcnt(12)
	v_mfma_f32_32x32x16_bf16 v[20:35], v[152:155], v[52:55], v[20:35]
	v_exp_f32_e32 v88, v88
	v_exp_f32_e32 v89, v89
	v_exp_f32_e32 v90, v90
	v_exp_f32_e32 v91, v91
	s_waitcnt lgkmcnt(10)
	v_mfma_f32_32x32x16_bf16 v[4:19], v[148:151], v[56:59], v[4:19]
	v_exp_f32_e32 v92, v92
	v_exp_f32_e32 v93, v93
	v_exp_f32_e32 v94, v94
	v_exp_f32_e32 v95, v95
	s_waitcnt lgkmcnt(8)
	v_mfma_f32_32x32x16_bf16 v[20:35], v[148:151], v[60:63], v[20:35]
	v_exp_f32_e32 v96, v96
	v_exp_f32_e32 v97, v97
	v_exp_f32_e32 v98, v98
	v_exp_f32_e32 v99, v99
	s_waitcnt vmcnt(2) lgkmcnt(0)
	s_barrier
	s_add_i32 s9, s28, 0x2000
	s_cmpk_lg_i32 s28, 0x4000
	s_cselect_b32 s30, s9, 0
	v_add_u32_e32 v194, s29, v187
	ds_read_b64_tr_b16 v[190:191], v194 offset:24576
	ds_read_b64_tr_b16 v[192:193], v194 offset:25088
	s_waitcnt lgkmcnt(9)
	v_mfma_f32_32x32x16_bf16 v[68:83], v[64:67], v[144:147], v[36:51]
	v_add_f32_e32 v52, v100, v101
	v_add_f32_e32 v52, v102, v52
	v_add_f32_e32 v52, v103, v52
	v_add_f32_e32 v52, v104, v52
	v_add_f32_e32 v52, v105, v52
	v_cvt_pk_bf16_f32 v160, v100, v101
	v_cvt_pk_bf16_f32 v161, v102, v103
	ds_read_b64_tr_b16 v[100:101], v194 offset:28672
	ds_read_b64_tr_b16 v[102:103], v194 offset:29184
	v_add_f32_e32 v52, v106, v52
	v_add_f32_e32 v52, v107, v52
	v_add_f32_e32 v52, v108, v52
	v_add_f32_e32 v148, v109, v52
	s_waitcnt lgkmcnt(10)
	v_mfma_f32_32x32x16_bf16 v[52:67], v[116:119], v[144:147], v[36:51]
	v_cvt_pk_bf16_f32 v162, v104, v105
	v_cvt_pk_bf16_f32 v163, v106, v107
	ds_read_b64_tr_b16 v[104:105], v194 offset:25600
	ds_read_b64_tr_b16 v[106:107], v194 offset:26112
	s_waitcnt lgkmcnt(11)
	v_mfma_f32_32x32x16_bf16 v[68:83], v[120:123], v[140:143], v[68:83]
	v_add_f32_e32 v116, v110, v148
	v_add_f32_e32 v116, v111, v116
	v_add_f32_e32 v116, v112, v116
	v_add_f32_e32 v116, v113, v116
	v_cvt_pk_bf16_f32 v156, v108, v109
	v_cvt_pk_bf16_f32 v157, v110, v111
	ds_read_b64_tr_b16 v[108:109], v194 offset:29696
	ds_read_b64_tr_b16 v[110:111], v194 offset:30208
	s_waitcnt lgkmcnt(12)
	v_mfma_f32_32x32x16_bf16 v[52:67], v[124:127], v[140:143], v[52:67]
	v_add_f32_e32 v116, v114, v116
	v_add_f32_e32 v116, v115, v116
	v_add_f32_e32 v116, v84, v116
	v_add_f32_e32 v116, v85, v116
	v_cvt_pk_bf16_f32 v158, v112, v113
	v_cvt_pk_bf16_f32 v159, v114, v115
	ds_read_b64_tr_b16 v[112:113], v194 offset:26624
	ds_read_b64_tr_b16 v[114:115], v194 offset:27136
	s_waitcnt lgkmcnt(13)
	v_mfma_f32_32x32x16_bf16 v[68:83], v[128:131], v[132:135], v[68:83]
	v_add_f32_e32 v116, v86, v116
	v_add_f32_e32 v116, v87, v116
	v_add_f32_e32 v116, v88, v116
	v_add_f32_e32 v116, v89, v116
	v_cvt_pk_bf16_f32 v152, v84, v85
	v_cvt_pk_bf16_f32 v153, v86, v87
	ds_read_b64_tr_b16 v[196:197], v194 offset:30720
	ds_read_b64_tr_b16 v[198:199], v194 offset:31232
	s_waitcnt lgkmcnt(14)
	v_mfma_f32_32x32x16_bf16 v[52:67], v[164:167], v[132:135], v[52:67]
	v_add_f32_e32 v84, v90, v116
	v_add_f32_e32 v84, v91, v84
	v_add_f32_e32 v84, v92, v84
	v_add_f32_e32 v84, v93, v84
	v_cvt_pk_bf16_f32 v154, v88, v89
	v_cvt_pk_bf16_f32 v155, v90, v91
	ds_read_b64_tr_b16 v[88:89], v194 offset:27648
	ds_read_b64_tr_b16 v[90:91], v194 offset:28160
	s_waitcnt lgkmcnt(14)
	v_mfma_f32_32x32x16_bf16 v[68:83], v[168:171], v[136:139], v[68:83]
	v_add_f32_e32 v84, v94, v84
	v_add_f32_e32 v84, v95, v84
	v_add_f32_e32 v84, v96, v84
	v_add_f32_e32 v84, v97, v84
	v_cvt_pk_bf16_f32 v148, v92, v93
	v_cvt_pk_bf16_f32 v149, v94, v95
	ds_read_b64_tr_b16 v[92:93], v194 offset:31744
	ds_read_b64_tr_b16 v[94:95], v194 offset:32256
	v_mfma_f32_32x32x16_bf16 v[52:67], v[172:175], v[136:139], v[52:67]
	v_add_f32_e32 v84, v98, v84
	v_add_f32_e32 v84, v99, v84
	v_add_f32_e32 v194, 0, v84
	v_cvt_pk_bf16_f32 v150, v96, v97
	v_cvt_pk_bf16_f32 v151, v98, v99
	v_lshl_add_u64 v[84:85], v[180:181], 0, s[4:5]
	s_add_i32 s9, s28, s20
	s_mov_b32 s29, m0
	s_mov_b32 m0, s9
	s_nop 0
	global_load_lds_dwordx4 v[84:85], off
	s_mov_b32 m0, s29
	v_lshl_add_u64 v[182:183], v[182:183], 0, s[6:7]
	s_add_i32 s9, s30, s8
	s_mov_b32 s29, m0
	s_mov_b32 m0, s9
	s_nop 0
	global_load_lds_dwordx4 v[182:183], off
	s_mov_b32 m0, s29
	s_waitcnt lgkmcnt(14)
	v_mfma_f32_32x32x16_bf16 v[4:19], v[160:163], v[190:193], v[4:19]
	v_exp_f32_e32 v68, v68
	v_exp_f32_e32 v69, v69
	v_exp_f32_e32 v70, v70
	v_exp_f32_e32 v71, v71
	s_waitcnt lgkmcnt(12)
	v_mfma_f32_32x32x16_bf16 v[20:35], v[160:163], v[100:103], v[20:35]
	v_exp_f32_e32 v72, v72
	v_exp_f32_e32 v73, v73
	v_exp_f32_e32 v74, v74
	v_exp_f32_e32 v75, v75
	v_add_u32_e32 v96, s30, v188
	ds_read_b128 v[84:87], v96
	ds_read_b128 v[172:175], v96 offset:512
	s_waitcnt lgkmcnt(12)
	v_mfma_f32_32x32x16_bf16 v[4:19], v[156:159], v[104:107], v[4:19]
	v_exp_f32_e32 v76, v76
	v_exp_f32_e32 v77, v77
	v_exp_f32_e32 v78, v78
	v_exp_f32_e32 v79, v79
	ds_read_b128 v[168:171], v96 offset:2048
	ds_read_b128 v[164:167], v96 offset:2560
	s_waitcnt lgkmcnt(12)
	v_mfma_f32_32x32x16_bf16 v[20:35], v[156:159], v[108:111], v[20:35]
	v_exp_f32_e32 v80, v80
	v_exp_f32_e32 v81, v81
	v_exp_f32_e32 v82, v82
	v_exp_f32_e32 v83, v83
	ds_read_b128 v[128:131], v96 offset:4096
	ds_read_b128 v[124:127], v96 offset:4608
	s_waitcnt lgkmcnt(12)
	v_mfma_f32_32x32x16_bf16 v[4:19], v[152:155], v[112:115], v[4:19]
	v_exp_f32_e32 v52, v52
	v_exp_f32_e32 v53, v53
	v_exp_f32_e32 v54, v54
	v_exp_f32_e32 v55, v55
	ds_read_b128 v[120:123], v96 offset:6144
	ds_read_b128 v[116:119], v96 offset:6656
	s_waitcnt lgkmcnt(12)
	v_mfma_f32_32x32x16_bf16 v[20:35], v[152:155], v[196:199], v[20:35]
	v_exp_f32_e32 v56, v56
	v_exp_f32_e32 v57, v57
	v_exp_f32_e32 v58, v58
	v_exp_f32_e32 v59, v59
	s_waitcnt lgkmcnt(10)
	v_mfma_f32_32x32x16_bf16 v[4:19], v[148:151], v[88:91], v[4:19]
	v_exp_f32_e32 v60, v60
	v_exp_f32_e32 v61, v61
	v_exp_f32_e32 v62, v62
	v_exp_f32_e32 v63, v63
	s_waitcnt lgkmcnt(8)
	v_mfma_f32_32x32x16_bf16 v[20:35], v[148:151], v[92:95], v[20:35]
	v_exp_f32_e32 v64, v64
	v_exp_f32_e32 v65, v65
	v_exp_f32_e32 v66, v66
	v_exp_f32_e32 v67, v67
	s_add_i32 s31, s30, 0x2000
	s_cmpk_lg_i32 s30, 0x4000
	v_add_f32_e32 v3, v3, v189
	s_mov_b32 s9, s28
	s_cselect_b32 s28, s31, 0
	s_add_i32 s27, s27, 2
	v_lshl_add_u64 v[180:181], v[180:181], 0, s[6:7]
	s_mov_b32 s29, s30
	v_add_f32_e32 v3, v3, v194
	s_cmp_gt_u32 s27, 24
	s_waitcnt vmcnt(2) lgkmcnt(0)
	s_barrier
	s_cbranch_scc0 .LBB1_142
	s_and_b32 s0, s21, 0x3fffffc0
	s_lshl_b32 s0, s0, 2
	s_add_i32 s4, s0, 0
	ds_read_b64_tr_b16 v[180:181], v187 offset:40960
	ds_read_b64_tr_b16 v[182:183], v187 offset:41472
	v_add_f32_e32 v88, v68, v69
	v_add_f32_e32 v88, v70, v88
	v_add_f32_e32 v88, v71, v88
	v_add_f32_e32 v88, v72, v88
	v_add_f32_e32 v88, v73, v88
	v_cvt_pk_bf16_f32 v160, v68, v69
	v_cvt_pk_bf16_f32 v161, v70, v71
	s_waitcnt lgkmcnt(9)
	v_mfma_f32_32x32x16_bf16 v[100:115], v[84:87], v[144:147], v[36:51]
	ds_read_b64_tr_b16 v[68:69], v187 offset:45056
	ds_read_b64_tr_b16 v[70:71], v187 offset:45568
	v_add_f32_e32 v84, v74, v88
	v_add_f32_e32 v84, v75, v84
	v_add_f32_e32 v84, v76, v84
	v_add_f32_e32 v148, v77, v84
	v_cvt_pk_bf16_f32 v162, v72, v73
	v_cvt_pk_bf16_f32 v163, v74, v75
	s_waitcnt lgkmcnt(10)
	v_mfma_f32_32x32x16_bf16 v[84:99], v[172:175], v[144:147], v[36:51]
	ds_read_b64_tr_b16 v[72:73], v187 offset:41984
	ds_read_b64_tr_b16 v[74:75], v187 offset:42496
	v_add_f32_e32 v148, v78, v148
	v_add_f32_e32 v148, v79, v148
	v_add_f32_e32 v148, v80, v148
	v_add_f32_e32 v148, v81, v148
	v_cvt_pk_bf16_f32 v156, v76, v77
	v_cvt_pk_bf16_f32 v157, v78, v79
	s_waitcnt lgkmcnt(11)
	v_mfma_f32_32x32x16_bf16 v[100:115], v[168:171], v[140:143], v[100:115]
	ds_read_b64_tr_b16 v[76:77], v187 offset:46080
	ds_read_b64_tr_b16 v[78:79], v187 offset:46592
	v_add_f32_e32 v148, v82, v148
	v_add_f32_e32 v148, v83, v148
	v_add_f32_e32 v148, v52, v148
	v_add_f32_e32 v148, v53, v148
	v_cvt_pk_bf16_f32 v158, v80, v81
	v_cvt_pk_bf16_f32 v159, v82, v83
	s_waitcnt lgkmcnt(12)
	v_mfma_f32_32x32x16_bf16 v[84:99], v[164:167], v[140:143], v[84:99]
	ds_read_b64_tr_b16 v[80:81], v187 offset:43008
	ds_read_b64_tr_b16 v[82:83], v187 offset:43520
	v_add_f32_e32 v148, v54, v148
	v_add_f32_e32 v148, v55, v148
	v_add_f32_e32 v148, v56, v148
	v_add_f32_e32 v148, v57, v148
	v_cvt_pk_bf16_f32 v152, v52, v53
	v_cvt_pk_bf16_f32 v153, v54, v55
	s_waitcnt lgkmcnt(13)
	v_mfma_f32_32x32x16_bf16 v[100:115], v[128:131], v[132:135], v[100:115]
	ds_read_b64_tr_b16 v[52:53], v187 offset:47104
	ds_read_b64_tr_b16 v[54:55], v187 offset:47616
	v_add_f32_e32 v128, v58, v148
	v_add_f32_e32 v128, v59, v128
	v_add_f32_e32 v128, v60, v128
	v_add_f32_e32 v128, v61, v128
	v_cvt_pk_bf16_f32 v154, v56, v57
	v_cvt_pk_bf16_f32 v155, v58, v59
	s_waitcnt lgkmcnt(14)
	v_mfma_f32_32x32x16_bf16 v[84:99], v[124:127], v[132:135], v[84:99]
	ds_read_b64_tr_b16 v[56:57], v187 offset:44032
	ds_read_b64_tr_b16 v[58:59], v187 offset:44544
	v_add_f32_e32 v124, v62, v128
	v_add_f32_e32 v124, v63, v124
	v_add_f32_e32 v124, v64, v124
	v_add_f32_e32 v124, v65, v124
	v_cvt_pk_bf16_f32 v148, v60, v61
	v_cvt_pk_bf16_f32 v149, v62, v63
	s_waitcnt lgkmcnt(14)
	v_mfma_f32_32x32x16_bf16 v[100:115], v[120:123], v[136:139], v[100:115]
	ds_read_b64_tr_b16 v[60:61], v187 offset:48128
	ds_read_b64_tr_b16 v[62:63], v187 offset:48640
	v_add_f32_e32 v120, v66, v124
	v_add_f32_e32 v120, v67, v120
	v_add_f32_e32 v120, 0, v120
	v_cvt_pk_bf16_f32 v150, v64, v65
	v_cvt_pk_bf16_f32 v151, v66, v67
	v_mfma_f32_32x32x16_bf16 v[84:99], v[116:119], v[136:139], v[84:99]
	s_mov_b64 s[0:1], 0x3c000
	s_cmp_lg_u32 0, -1
	v_lshl_add_u64 v[64:65], v[178:179], 0, s[0:1]
	s_mov_b32 s2, m0
	s_mov_b32 m0, s20
	s_nop 0
	global_load_lds_dwordx4 v[64:65], off
	s_mov_b32 m0, s2
	s_cselect_b32 s7, 0, 0
	s_mov_b64 s[2:3], 0x38000
	s_add_i32 s5, s7, 0x8000
	v_lshl_add_u64 v[64:65], v[176:177], 0, s[2:3]
	s_add_i32 s6, s11, s5
	s_mov_b32 s2, m0
	s_mov_b32 m0, s6
	s_nop 0
	global_load_lds_dwordx4 v[64:65], off
	s_mov_b32 m0, s2
	v_add_f32_e32 v3, v3, v120
	s_waitcnt lgkmcnt(14)
	v_mfma_f32_32x32x16_bf16 v[4:19], v[160:163], v[180:183], v[4:19]
	v_exp_f32_e32 v100, v100
	v_exp_f32_e32 v101, v101
	v_exp_f32_e32 v102, v102
	v_exp_f32_e32 v103, v103
	s_waitcnt lgkmcnt(12)
	v_mfma_f32_32x32x16_bf16 v[20:35], v[160:163], v[68:71], v[20:35]
	v_exp_f32_e32 v104, v104
	v_exp_f32_e32 v105, v105
	v_exp_f32_e32 v106, v106
	v_exp_f32_e32 v107, v107
	ds_read_b128 v[64:67], v188 offset:8192
	ds_read_b128 v[68:71], v188 offset:8704
	s_waitcnt lgkmcnt(12)
	v_mfma_f32_32x32x16_bf16 v[4:19], v[156:159], v[72:75], v[4:19]
	v_exp_f32_e32 v108, v108
	v_exp_f32_e32 v109, v109
	v_exp_f32_e32 v110, v110
	v_exp_f32_e32 v111, v111
	ds_read_b128 v[72:75], v188 offset:10240
	ds_read_b128 v[164:167], v188 offset:10752
	s_waitcnt lgkmcnt(12)
	v_mfma_f32_32x32x16_bf16 v[20:35], v[156:159], v[76:79], v[20:35]
	v_exp_f32_e32 v112, v112
	v_exp_f32_e32 v113, v113
	v_exp_f32_e32 v114, v114
	v_exp_f32_e32 v115, v115
	ds_read_b128 v[76:79], v188 offset:12288
	ds_read_b128 v[168:171], v188 offset:12800
	s_waitcnt lgkmcnt(12)
	v_mfma_f32_32x32x16_bf16 v[4:19], v[152:155], v[80:83], v[4:19]
	v_exp_f32_e32 v84, v84
	v_exp_f32_e32 v85, v85
	v_exp_f32_e32 v86, v86
	v_exp_f32_e32 v87, v87
	ds_read_b128 v[80:83], v188 offset:14336
	ds_read_b128 v[172:175], v188 offset:14848
	s_waitcnt lgkmcnt(12)
	v_mfma_f32_32x32x16_bf16 v[20:35], v[152:155], v[52:55], v[20:35]
	v_exp_f32_e32 v88, v88
	v_exp_f32_e32 v89, v89
	v_exp_f32_e32 v90, v90
	v_exp_f32_e32 v91, v91
	s_waitcnt lgkmcnt(10)
	v_mfma_f32_32x32x16_bf16 v[4:19], v[148:151], v[56:59], v[4:19]
	v_exp_f32_e32 v92, v92
	v_exp_f32_e32 v93, v93
	v_exp_f32_e32 v94, v94
	v_exp_f32_e32 v95, v95
	s_waitcnt lgkmcnt(8)
	v_mfma_f32_32x32x16_bf16 v[20:35], v[148:151], v[60:63], v[20:35]
	v_exp_f32_e32 v96, v96
	v_exp_f32_e32 v97, v97
	v_exp_f32_e32 v98, v98
	v_exp_f32_e32 v99, v99
	s_waitcnt vmcnt(2) lgkmcnt(0)
	s_barrier
	ds_read_b64_tr_b16 v[180:181], v187 offset:24576
	ds_read_b64_tr_b16 v[182:183], v187 offset:25088
	v_add_f32_e32 v52, v100, v101
	v_add_f32_e32 v52, v102, v52
	v_add_f32_e32 v52, v103, v52
	v_add_f32_e32 v52, v104, v52
	v_add_f32_e32 v52, v105, v52
	v_cvt_pk_bf16_f32 v160, v100, v101
	v_cvt_pk_bf16_f32 v161, v102, v103
	s_waitcnt lgkmcnt(9)
	v_mfma_f32_32x32x16_bf16 v[116:131], v[64:67], v[144:147], v[36:51]
	ds_read_b64_tr_b16 v[100:101], v187 offset:28672
	ds_read_b64_tr_b16 v[102:103], v187 offset:29184
	v_add_f32_e32 v52, v106, v52
	v_add_f32_e32 v52, v107, v52
	v_add_f32_e32 v52, v108, v52
	v_add_f32_e32 v148, v109, v52
	v_cvt_pk_bf16_f32 v162, v104, v105
	v_cvt_pk_bf16_f32 v163, v106, v107
	s_waitcnt lgkmcnt(10)
	v_mfma_f32_32x32x16_bf16 v[52:67], v[68:71], v[144:147], v[36:51]
	ds_read_b64_tr_b16 v[68:69], v187 offset:25600
	ds_read_b64_tr_b16 v[70:71], v187 offset:26112
	v_add_f32_e32 v104, v110, v148
	v_add_f32_e32 v104, v111, v104
	v_add_f32_e32 v104, v112, v104
	v_add_f32_e32 v104, v113, v104
	v_cvt_pk_bf16_f32 v156, v108, v109
	v_cvt_pk_bf16_f32 v157, v110, v111
	s_waitcnt lgkmcnt(11)
	v_mfma_f32_32x32x16_bf16 v[116:131], v[72:75], v[140:143], v[116:131]
	ds_read_b64_tr_b16 v[72:73], v187 offset:29696
	ds_read_b64_tr_b16 v[74:75], v187 offset:30208
	v_add_f32_e32 v104, v114, v104
	v_add_f32_e32 v104, v115, v104
	v_add_f32_e32 v104, v84, v104
	v_add_f32_e32 v108, v85, v104
	v_cvt_pk_bf16_f32 v158, v112, v113
	v_cvt_pk_bf16_f32 v159, v114, v115
	s_waitcnt lgkmcnt(12)
	v_mfma_f32_32x32x16_bf16 v[52:67], v[164:167], v[140:143], v[52:67]
	ds_read_b64_tr_b16 v[104:105], v187 offset:26624
	ds_read_b64_tr_b16 v[106:107], v187 offset:27136
	v_add_f32_e32 v108, v86, v108
	v_add_f32_e32 v108, v87, v108
	v_add_f32_e32 v108, v88, v108
	v_add_f32_e32 v108, v89, v108
	v_cvt_pk_bf16_f32 v152, v84, v85
	v_cvt_pk_bf16_f32 v153, v86, v87
	s_waitcnt lgkmcnt(13)
	v_mfma_f32_32x32x16_bf16 v[116:131], v[76:79], v[132:135], v[116:131]
	ds_read_b64_tr_b16 v[76:77], v187 offset:30720
	ds_read_b64_tr_b16 v[78:79], v187 offset:31232
	v_add_f32_e32 v84, v90, v108
	v_add_f32_e32 v84, v91, v84
	v_add_f32_e32 v84, v92, v84
	v_add_f32_e32 v108, v93, v84
	v_cvt_pk_bf16_f32 v154, v88, v89
	v_cvt_pk_bf16_f32 v155, v90, v91
	s_waitcnt lgkmcnt(14)
	v_mfma_f32_32x32x16_bf16 v[52:67], v[168:171], v[132:135], v[52:67]
	ds_read_b64_tr_b16 v[84:85], v187 offset:27648
	ds_read_b64_tr_b16 v[86:87], v187 offset:28160
	v_add_f32_e32 v88, v94, v108
	v_add_f32_e32 v88, v95, v88
	v_add_f32_e32 v88, v96, v88
	v_add_f32_e32 v88, v97, v88
	v_cvt_pk_bf16_f32 v148, v92, v93
	v_cvt_pk_bf16_f32 v149, v94, v95
	s_waitcnt lgkmcnt(14)
	v_mfma_f32_32x32x16_bf16 v[116:131], v[80:83], v[136:139], v[116:131]
	ds_read_b64_tr_b16 v[80:81], v187 offset:31744
	ds_read_b64_tr_b16 v[82:83], v187 offset:32256
	v_add_f32_e32 v88, v98, v88
	v_add_f32_e32 v88, v99, v88
	v_add_f32_e32 v88, 0, v88
	v_cvt_pk_bf16_f32 v150, v96, v97
	v_cvt_pk_bf16_f32 v151, v98, v99
	v_mfma_f32_32x32x16_bf16 v[52:67], v[172:175], v[136:139], v[52:67]
	s_mov_b64 s[2:3], 0x3e000
	s_add_i32 s7, s7, s11
	v_add_f32_e32 v3, v3, v88
	v_lshl_add_u64 v[88:89], v[178:179], 0, s[2:3]
	s_add_i32 s9, s7, 0x2000
	s_mov_b32 s11, m0
	s_mov_b32 m0, s9
	s_nop 0
	global_load_lds_dwordx4 v[88:89], off
	s_mov_b32 m0, s11
	s_mov_b64 s[20:21], 0x3a000
	v_lshl_add_u64 v[88:89], v[176:177], 0, s[20:21]
	s_add_i32 s7, s7, 0xa000
	s_mov_b32 s9, m0
	s_mov_b32 m0, s7
	s_nop 0
	global_load_lds_dwordx4 v[88:89], off
	s_mov_b32 m0, s9
	s_waitcnt lgkmcnt(14)
	v_mfma_f32_32x32x16_bf16 v[4:19], v[160:163], v[180:183], v[4:19]
	v_exp_f32_e32 v116, v116
	v_exp_f32_e32 v117, v117
	v_exp_f32_e32 v118, v118
	v_exp_f32_e32 v119, v119
	s_waitcnt lgkmcnt(12)
	v_mfma_f32_32x32x16_bf16 v[20:35], v[160:163], v[100:103], v[20:35]
	v_exp_f32_e32 v120, v120
	v_exp_f32_e32 v121, v121
	v_exp_f32_e32 v122, v122
	v_exp_f32_e32 v123, v123
	ds_read_b128 v[100:103], v188 offset:16384
	ds_read_b128 v[108:111], v188 offset:16896
	s_waitcnt lgkmcnt(12)
	v_mfma_f32_32x32x16_bf16 v[4:19], v[156:159], v[68:71], v[4:19]
	v_exp_f32_e32 v124, v124
	v_exp_f32_e32 v125, v125
	v_exp_f32_e32 v126, v126
	v_exp_f32_e32 v127, v127
	ds_read_b128 v[112:115], v188 offset:18432
	ds_read_b128 v[164:167], v188 offset:18944
	s_waitcnt lgkmcnt(12)
	v_mfma_f32_32x32x16_bf16 v[20:35], v[156:159], v[72:75], v[20:35]
	v_exp_f32_e32 v128, v128
	v_exp_f32_e32 v129, v129
	v_exp_f32_e32 v130, v130
	v_exp_f32_e32 v131, v131
	ds_read_b128 v[168:171], v188 offset:20480
	ds_read_b128 v[172:175], v188 offset:20992
	s_waitcnt lgkmcnt(12)
	v_mfma_f32_32x32x16_bf16 v[4:19], v[152:155], v[104:107], v[4:19]
	v_exp_f32_e32 v52, v52
	v_exp_f32_e32 v53, v53
	v_exp_f32_e32 v54, v54
	v_exp_f32_e32 v55, v55
	ds_read_b128 v[104:107], v188 offset:22528
	ds_read_b128 v[178:181], v188 offset:23040
	s_waitcnt lgkmcnt(12)
	v_mfma_f32_32x32x16_bf16 v[20:35], v[152:155], v[76:79], v[20:35]
	v_exp_f32_e32 v56, v56
	v_exp_f32_e32 v57, v57
	v_exp_f32_e32 v58, v58
	v_exp_f32_e32 v59, v59
	s_waitcnt lgkmcnt(10)
	v_mfma_f32_32x32x16_bf16 v[4:19], v[148:151], v[84:87], v[4:19]
	v_exp_f32_e32 v60, v60
	v_exp_f32_e32 v61, v61
	v_exp_f32_e32 v62, v62
	v_exp_f32_e32 v63, v63
	s_waitcnt lgkmcnt(8)
	v_mfma_f32_32x32x16_bf16 v[20:35], v[148:151], v[80:83], v[20:35]
	v_exp_f32_e32 v64, v64
	v_exp_f32_e32 v65, v65
	v_exp_f32_e32 v66, v66
	v_exp_f32_e32 v67, v67
	s_waitcnt vmcnt(2) lgkmcnt(0)
	s_barrier
	ds_read_b64_tr_b16 v[190:191], v187 offset:32768
	ds_read_b64_tr_b16 v[192:193], v187 offset:33280
	v_add_f32_e32 v68, v116, v117
	v_add_f32_e32 v68, v118, v68
	v_add_f32_e32 v68, v119, v68
	v_add_f32_e32 v68, v120, v68
	v_add_f32_e32 v68, v121, v68
	v_cvt_pk_bf16_f32 v160, v116, v117
	v_cvt_pk_bf16_f32 v161, v118, v119
	s_waitcnt lgkmcnt(9)
	v_mfma_f32_32x32x16_bf16 v[84:99], v[100:103], v[144:147], v[36:51]
	ds_read_b64_tr_b16 v[100:101], v187 offset:36864
	ds_read_b64_tr_b16 v[102:103], v187 offset:37376
	v_add_f32_e32 v68, v122, v68
	v_add_f32_e32 v68, v123, v68
	v_add_f32_e32 v68, v124, v68
	v_add_f32_e32 v116, v125, v68
	v_cvt_pk_bf16_f32 v162, v120, v121
	v_cvt_pk_bf16_f32 v163, v122, v123
	s_waitcnt lgkmcnt(10)
	v_mfma_f32_32x32x16_bf16 v[68:83], v[108:111], v[144:147], v[36:51]
	ds_read_b64_tr_b16 v[108:109], v187 offset:33792
	ds_read_b64_tr_b16 v[110:111], v187 offset:34304
	v_add_f32_e32 v116, v126, v116
	v_add_f32_e32 v116, v127, v116
	v_add_f32_e32 v116, v128, v116
	v_add_f32_e32 v116, v129, v116
	v_cvt_pk_bf16_f32 v156, v124, v125
	v_cvt_pk_bf16_f32 v157, v126, v127
	s_waitcnt lgkmcnt(11)
	v_mfma_f32_32x32x16_bf16 v[84:99], v[112:115], v[140:143], v[84:99]
	ds_read_b64_tr_b16 v[112:113], v187 offset:37888
	ds_read_b64_tr_b16 v[114:115], v187 offset:38400
	v_add_f32_e32 v116, v130, v116
	v_add_f32_e32 v116, v131, v116
	v_add_f32_e32 v116, v52, v116
	v_add_f32_e32 v120, v53, v116
	v_cvt_pk_bf16_f32 v158, v128, v129
	v_cvt_pk_bf16_f32 v159, v130, v131
	s_waitcnt lgkmcnt(12)
	v_mfma_f32_32x32x16_bf16 v[68:83], v[164:167], v[140:143], v[68:83]
	ds_read_b64_tr_b16 v[116:117], v187 offset:34816
	ds_read_b64_tr_b16 v[118:119], v187 offset:35328
	v_add_f32_e32 v120, v54, v120
	v_add_f32_e32 v120, v55, v120
	v_add_f32_e32 v120, v56, v120
	v_add_f32_e32 v120, v57, v120
	v_cvt_pk_bf16_f32 v152, v52, v53
	v_cvt_pk_bf16_f32 v153, v54, v55
	s_waitcnt lgkmcnt(13)
	v_mfma_f32_32x32x16_bf16 v[84:99], v[168:171], v[132:135], v[84:99]
	ds_read_b64_tr_b16 v[52:53], v187 offset:38912
	ds_read_b64_tr_b16 v[54:55], v187 offset:39424
	v_add_f32_e32 v120, v58, v120
	v_add_f32_e32 v120, v59, v120
	v_add_f32_e32 v120, v60, v120
	v_add_f32_e32 v120, v61, v120
	v_cvt_pk_bf16_f32 v154, v56, v57
	v_cvt_pk_bf16_f32 v155, v58, v59
	s_waitcnt lgkmcnt(14)
	v_mfma_f32_32x32x16_bf16 v[68:83], v[172:175], v[132:135], v[68:83]
	ds_read_b64_tr_b16 v[56:57], v187 offset:35840
	ds_read_b64_tr_b16 v[58:59], v187 offset:36352
	v_add_f32_e32 v120, v62, v120
	v_add_f32_e32 v120, v63, v120
	v_add_f32_e32 v120, v64, v120
	v_add_f32_e32 v120, v65, v120
	v_cvt_pk_bf16_f32 v148, v60, v61
	v_cvt_pk_bf16_f32 v149, v62, v63
	s_waitcnt lgkmcnt(14)
	v_mfma_f32_32x32x16_bf16 v[84:99], v[104:107], v[136:139], v[84:99]
	ds_read_b64_tr_b16 v[60:61], v187 offset:39936
	ds_read_b64_tr_b16 v[62:63], v187 offset:40448
	v_add_f32_e32 v104, v66, v120
	v_add_f32_e32 v104, v67, v104
	v_add_f32_e32 v104, 0, v104
	v_cvt_pk_bf16_f32 v150, v64, v65
	v_cvt_pk_bf16_f32 v151, v66, v67
	v_mfma_f32_32x32x16_bf16 v[68:83], v[178:181], v[136:139], v[68:83]
	v_lshl_add_u64 v[64:65], v[176:177], 0, s[0:1]
	s_mov_b32 s0, m0
	s_mov_b32 m0, s8
	s_nop 0
	global_load_lds_dwordx4 v[64:65], off
	s_mov_b32 m0, s0
	v_add_f32_e32 v3, v3, v104
	s_waitcnt lgkmcnt(14)
	v_mfma_f32_32x32x16_bf16 v[4:19], v[160:163], v[190:193], v[4:19]
	v_exp_f32_e32 v84, v84
	v_exp_f32_e32 v85, v85
	v_exp_f32_e32 v86, v86
	v_exp_f32_e32 v87, v87
	s_waitcnt lgkmcnt(12)
	v_mfma_f32_32x32x16_bf16 v[20:35], v[160:163], v[100:103], v[20:35]
	v_exp_f32_e32 v88, v88
	v_exp_f32_e32 v89, v89
	v_exp_f32_e32 v90, v90
	v_exp_f32_e32 v91, v91
	ds_read_b128 v[64:67], v188
	ds_read_b128 v[120:123], v188 offset:512
	s_waitcnt lgkmcnt(12)
	v_mfma_f32_32x32x16_bf16 v[4:19], v[156:159], v[108:111], v[4:19]
	v_exp_f32_e32 v92, v92
	v_exp_f32_e32 v93, v93
	v_exp_f32_e32 v94, v94
	v_exp_f32_e32 v95, v95
	ds_read_b128 v[124:127], v188 offset:2048
	ds_read_b128 v[128:131], v188 offset:2560
	s_waitcnt lgkmcnt(12)
	v_mfma_f32_32x32x16_bf16 v[20:35], v[156:159], v[112:115], v[20:35]
	v_exp_f32_e32 v96, v96
	v_exp_f32_e32 v97, v97
	v_exp_f32_e32 v98, v98
	v_exp_f32_e32 v99, v99
	ds_read_b128 v[164:167], v188 offset:4096
	ds_read_b128 v[168:171], v188 offset:4608
	s_waitcnt lgkmcnt(12)
	v_mfma_f32_32x32x16_bf16 v[4:19], v[152:155], v[116:119], v[4:19]
	v_exp_f32_e32 v68, v68
	v_exp_f32_e32 v69, v69
	v_exp_f32_e32 v70, v70
	v_exp_f32_e32 v71, v71
	ds_read_b128 v[116:119], v188 offset:6144
	ds_read_b128 v[172:175], v188 offset:6656
	s_waitcnt lgkmcnt(12)
	v_mfma_f32_32x32x16_bf16 v[20:35], v[152:155], v[52:55], v[20:35]
	v_exp_f32_e32 v72, v72
	v_exp_f32_e32 v73, v73
	v_exp_f32_e32 v74, v74
	v_exp_f32_e32 v75, v75
	s_waitcnt lgkmcnt(10)
	v_mfma_f32_32x32x16_bf16 v[4:19], v[148:151], v[56:59], v[4:19]
	v_exp_f32_e32 v76, v76
	v_exp_f32_e32 v77, v77
	v_exp_f32_e32 v78, v78
	v_exp_f32_e32 v79, v79
	s_waitcnt lgkmcnt(8)
	v_mfma_f32_32x32x16_bf16 v[20:35], v[148:151], v[60:63], v[20:35]
	v_exp_f32_e32 v80, v80
	v_exp_f32_e32 v81, v81
	v_exp_f32_e32 v82, v82
	v_exp_f32_e32 v83, v83
	s_waitcnt vmcnt(1) lgkmcnt(0)
	s_barrier
	ds_read_b64_tr_b16 v[178:179], v187 offset:40960
	ds_read_b64_tr_b16 v[180:181], v187 offset:41472
	v_add_f32_e32 v52, v84, v85
	v_add_f32_e32 v52, v86, v52
	v_add_f32_e32 v52, v87, v52
	v_add_f32_e32 v52, v88, v52
	v_add_f32_e32 v52, v89, v52
	v_cvt_pk_bf16_f32 v160, v84, v85
	v_cvt_pk_bf16_f32 v161, v86, v87
	s_waitcnt lgkmcnt(9)
	v_mfma_f32_32x32x16_bf16 v[100:115], v[64:67], v[144:147], v[36:51]
	ds_read_b64_tr_b16 v[84:85], v187 offset:45056
	ds_read_b64_tr_b16 v[86:87], v187 offset:45568
	v_add_f32_e32 v52, v90, v52
	v_add_f32_e32 v52, v91, v52
	v_add_f32_e32 v52, v92, v52
	v_add_f32_e32 v148, v93, v52
	v_cvt_pk_bf16_f32 v162, v88, v89
	v_cvt_pk_bf16_f32 v163, v90, v91
	s_waitcnt lgkmcnt(10)
	v_mfma_f32_32x32x16_bf16 v[52:67], v[120:123], v[144:147], v[36:51]
	ds_read_b64_tr_b16 v[88:89], v187 offset:41984
	ds_read_b64_tr_b16 v[90:91], v187 offset:42496
	v_add_f32_e32 v120, v94, v148
	v_add_f32_e32 v120, v95, v120
	v_add_f32_e32 v120, v96, v120
	v_add_f32_e32 v120, v97, v120
	v_cvt_pk_bf16_f32 v156, v92, v93
	v_cvt_pk_bf16_f32 v157, v94, v95
	s_waitcnt lgkmcnt(11)
	v_mfma_f32_32x32x16_bf16 v[100:115], v[124:127], v[140:143], v[100:115]
	ds_read_b64_tr_b16 v[92:93], v187 offset:46080
	ds_read_b64_tr_b16 v[94:95], v187 offset:46592
	v_add_f32_e32 v120, v98, v120
	v_add_f32_e32 v120, v99, v120
	v_add_f32_e32 v120, v68, v120
	v_add_f32_e32 v120, v69, v120
	v_cvt_pk_bf16_f32 v158, v96, v97
	v_cvt_pk_bf16_f32 v159, v98, v99
	s_waitcnt lgkmcnt(12)
	v_mfma_f32_32x32x16_bf16 v[52:67], v[128:131], v[140:143], v[52:67]
	ds_read_b64_tr_b16 v[96:97], v187 offset:43008
	ds_read_b64_tr_b16 v[98:99], v187 offset:43520
	v_add_f32_e32 v120, v70, v120
	v_add_f32_e32 v120, v71, v120
	v_add_f32_e32 v120, v72, v120
	v_add_f32_e32 v120, v73, v120
	v_cvt_pk_bf16_f32 v152, v68, v69
	v_cvt_pk_bf16_f32 v153, v70, v71
	s_waitcnt lgkmcnt(13)
	v_mfma_f32_32x32x16_bf16 v[100:115], v[164:167], v[132:135], v[100:115]
	ds_read_b64_tr_b16 v[68:69], v187 offset:47104
	ds_read_b64_tr_b16 v[70:71], v187 offset:47616
	v_add_f32_e32 v120, v74, v120
	v_add_f32_e32 v120, v75, v120
	v_add_f32_e32 v120, v76, v120
	v_add_f32_e32 v120, v77, v120
	v_cvt_pk_bf16_f32 v154, v72, v73
	v_cvt_pk_bf16_f32 v155, v74, v75
	s_waitcnt lgkmcnt(14)
	v_mfma_f32_32x32x16_bf16 v[52:67], v[168:171], v[132:135], v[52:67]
	ds_read_b64_tr_b16 v[72:73], v187 offset:44032
	ds_read_b64_tr_b16 v[74:75], v187 offset:44544
	v_add_f32_e32 v120, v78, v120
	v_add_f32_e32 v120, v79, v120
	v_add_f32_e32 v120, v80, v120
	v_add_f32_e32 v120, v81, v120
	v_cvt_pk_bf16_f32 v148, v76, v77
	v_cvt_pk_bf16_f32 v149, v78, v79
	s_waitcnt lgkmcnt(14)
	v_mfma_f32_32x32x16_bf16 v[100:115], v[116:119], v[136:139], v[100:115]
	ds_read_b64_tr_b16 v[76:77], v187 offset:48128
	ds_read_b64_tr_b16 v[78:79], v187 offset:48640
	v_add_f32_e32 v116, v82, v120
	v_add_f32_e32 v116, v83, v116
	v_add_f32_e32 v116, 0, v116
	v_cvt_pk_bf16_f32 v150, v80, v81
	v_cvt_pk_bf16_f32 v151, v82, v83
	v_mfma_f32_32x32x16_bf16 v[52:67], v[172:175], v[136:139], v[52:67]
	v_lshl_add_u64 v[80:81], v[176:177], 0, s[2:3]
	s_mov_b32 s0, m0
	s_mov_b32 m0, s6
	s_nop 0
	global_load_lds_dwordx4 v[80:81], off
	s_mov_b32 m0, s0
	v_add_f32_e32 v3, v3, v116
	s_waitcnt lgkmcnt(14)
	v_mfma_f32_32x32x16_bf16 v[4:19], v[160:163], v[178:181], v[4:19]
	v_exp_f32_e32 v100, v100
	v_exp_f32_e32 v101, v101
	v_exp_f32_e32 v102, v102
	v_exp_f32_e32 v103, v103
	s_waitcnt lgkmcnt(12)
	v_mfma_f32_32x32x16_bf16 v[20:35], v[160:163], v[84:87], v[20:35]
	v_exp_f32_e32 v104, v104
	v_exp_f32_e32 v105, v105
	v_exp_f32_e32 v106, v106
	v_exp_f32_e32 v107, v107
	ds_read_b128 v[84:87], v188 offset:8192
	ds_read_b128 v[116:119], v188 offset:8704
	s_waitcnt lgkmcnt(12)
	v_mfma_f32_32x32x16_bf16 v[4:19], v[156:159], v[88:91], v[4:19]
	v_exp_f32_e32 v108, v108
	v_exp_f32_e32 v109, v109
	v_exp_f32_e32 v110, v110
	v_exp_f32_e32 v111, v111
	ds_read_b128 v[88:91], v188 offset:10240
	ds_read_b128 v[120:123], v188 offset:10752
	s_waitcnt lgkmcnt(12)
	v_mfma_f32_32x32x16_bf16 v[20:35], v[156:159], v[92:95], v[20:35]
	v_exp_f32_e32 v112, v112
	v_exp_f32_e32 v113, v113
	v_exp_f32_e32 v114, v114
	v_exp_f32_e32 v115, v115
	ds_read_b128 v[92:95], v188 offset:12288
	ds_read_b128 v[124:127], v188 offset:12800
	s_waitcnt lgkmcnt(12)
	v_mfma_f32_32x32x16_bf16 v[4:19], v[152:155], v[96:99], v[4:19]
	v_exp_f32_e32 v52, v52
	v_exp_f32_e32 v53, v53
	v_exp_f32_e32 v54, v54
	v_exp_f32_e32 v55, v55
	ds_read_b128 v[96:99], v188 offset:14336
	ds_read_b128 v[128:131], v188 offset:14848
	s_waitcnt lgkmcnt(12)
	v_mfma_f32_32x32x16_bf16 v[20:35], v[152:155], v[68:71], v[20:35]
	v_exp_f32_e32 v56, v56
	v_exp_f32_e32 v57, v57
	v_exp_f32_e32 v58, v58
	v_exp_f32_e32 v59, v59
	s_waitcnt lgkmcnt(10)
	v_mfma_f32_32x32x16_bf16 v[4:19], v[148:151], v[72:75], v[4:19]
	v_exp_f32_e32 v60, v60
	v_exp_f32_e32 v61, v61
	v_exp_f32_e32 v62, v62
	v_exp_f32_e32 v63, v63
	s_waitcnt lgkmcnt(8)
	v_mfma_f32_32x32x16_bf16 v[20:35], v[148:151], v[76:79], v[20:35]
	v_exp_f32_e32 v64, v64
	v_exp_f32_e32 v65, v65
	v_exp_f32_e32 v66, v66
	v_exp_f32_e32 v67, v67
	s_waitcnt vmcnt(0) lgkmcnt(0)
	s_barrier
	ds_read_b64_tr_b16 v[164:165], v187 offset:24576
	ds_read_b64_tr_b16 v[166:167], v187 offset:25088
	v_add_f32_e32 v68, v100, v101
	v_add_f32_e32 v68, v102, v68
	v_add_f32_e32 v68, v103, v68
	v_add_f32_e32 v68, v104, v68
	v_add_f32_e32 v148, v105, v68
	v_cvt_pk_bf16_f32 v160, v100, v101
	v_cvt_pk_bf16_f32 v161, v102, v103
	s_waitcnt lgkmcnt(9)
	v_mfma_f32_32x32x16_bf16 v[68:83], v[84:87], v[144:147], v[36:51]
	ds_read_b64_tr_b16 v[84:85], v187 offset:28672
	ds_read_b64_tr_b16 v[86:87], v187 offset:29184
	s_waitcnt lgkmcnt(10)
	v_mfma_f32_32x32x16_bf16 v[36:51], v[116:119], v[144:147], v[36:51]
	v_add_f32_e32 v100, v106, v148
	v_add_f32_e32 v100, v107, v100
	v_add_f32_e32 v100, v108, v100
	v_add_f32_e32 v148, v109, v100
	v_cvt_pk_bf16_f32 v162, v104, v105
	v_cvt_pk_bf16_f32 v163, v106, v107
	ds_read_b64_tr_b16 v[100:101], v187 offset:25600
	ds_read_b64_tr_b16 v[102:103], v187 offset:26112
	v_add_f32_e32 v104, v110, v148
	v_add_f32_e32 v104, v111, v104
	v_add_f32_e32 v104, v112, v104
	v_add_f32_e32 v104, v113, v104
	v_cvt_pk_bf16_f32 v156, v108, v109
	v_cvt_pk_bf16_f32 v157, v110, v111
	s_waitcnt lgkmcnt(11)
	v_mfma_f32_32x32x16_bf16 v[68:83], v[88:91], v[140:143], v[68:83]
	ds_read_b64_tr_b16 v[88:89], v187 offset:29696
	ds_read_b64_tr_b16 v[90:91], v187 offset:30208
	s_waitcnt lgkmcnt(12)
	v_mfma_f32_32x32x16_bf16 v[36:51], v[120:123], v[140:143], v[36:51]
	v_add_f32_e32 v104, v114, v104
	v_add_f32_e32 v104, v115, v104
	v_add_f32_e32 v104, v52, v104
	v_add_f32_e32 v108, v53, v104
	v_cvt_pk_bf16_f32 v158, v112, v113
	v_cvt_pk_bf16_f32 v159, v114, v115
	ds_read_b64_tr_b16 v[104:105], v187 offset:26624
	ds_read_b64_tr_b16 v[106:107], v187 offset:27136
	v_add_f32_e32 v108, v54, v108
	v_add_f32_e32 v108, v55, v108
	v_add_f32_e32 v108, v56, v108
	v_add_f32_e32 v108, v57, v108
	v_cvt_pk_bf16_f32 v152, v52, v53
	v_cvt_pk_bf16_f32 v153, v54, v55
	s_waitcnt lgkmcnt(13)
	v_mfma_f32_32x32x16_bf16 v[68:83], v[92:95], v[132:135], v[68:83]
	ds_read_b64_tr_b16 v[52:53], v187 offset:30720
	ds_read_b64_tr_b16 v[54:55], v187 offset:31232
	s_waitcnt lgkmcnt(14)
	v_mfma_f32_32x32x16_bf16 v[36:51], v[124:127], v[132:135], v[36:51]
	v_add_f32_e32 v92, v58, v108
	v_add_f32_e32 v92, v59, v92
	v_add_f32_e32 v92, v60, v92
	v_add_f32_e32 v92, v61, v92
	v_cvt_pk_bf16_f32 v154, v56, v57
	v_cvt_pk_bf16_f32 v155, v58, v59
	ds_read_b64_tr_b16 v[56:57], v187 offset:27648
	ds_read_b64_tr_b16 v[58:59], v187 offset:28160
	v_add_f32_e32 v92, v62, v92
	v_add_f32_e32 v92, v63, v92
	v_add_f32_e32 v92, v64, v92
	v_add_f32_e32 v92, v65, v92
	v_cvt_pk_bf16_f32 v148, v60, v61
	v_cvt_pk_bf16_f32 v149, v62, v63
	s_waitcnt lgkmcnt(14)
	v_mfma_f32_32x32x16_bf16 v[68:83], v[96:99], v[136:139], v[68:83]
	ds_read_b64_tr_b16 v[60:61], v187 offset:31744
	ds_read_b64_tr_b16 v[62:63], v187 offset:32256
	v_mfma_f32_32x32x16_bf16 v[36:51], v[128:131], v[136:139], v[36:51]
	v_add_f32_e32 v92, v66, v92
	v_add_f32_e32 v92, v67, v92
	v_add_f32_e32 v92, 0, v92
	v_cvt_pk_bf16_f32 v150, v64, v65
	v_cvt_pk_bf16_f32 v151, v66, v67
	s_nop 0
	v_add_f32_e32 v3, v3, v92
	s_waitcnt lgkmcnt(14)
	v_mfma_f32_32x32x16_bf16 v[4:19], v[160:163], v[164:167], v[4:19]
	v_exp_f32_e32 v68, v68
	v_exp_f32_e32 v69, v69
	v_exp_f32_e32 v70, v70
	v_exp_f32_e32 v71, v71
	s_waitcnt lgkmcnt(12)
	v_mfma_f32_32x32x16_bf16 v[20:35], v[160:163], v[84:87], v[20:35]
	v_exp_f32_e32 v72, v72
	v_exp_f32_e32 v73, v73
	v_exp_f32_e32 v74, v74
	v_exp_f32_e32 v75, v75
	s_waitcnt lgkmcnt(10)
	v_mfma_f32_32x32x16_bf16 v[4:19], v[156:159], v[100:103], v[4:19]
	v_exp_f32_e32 v76, v76
	v_exp_f32_e32 v77, v77
	v_exp_f32_e32 v78, v78
	v_exp_f32_e32 v79, v79
	s_waitcnt lgkmcnt(8)
	v_mfma_f32_32x32x16_bf16 v[20:35], v[156:159], v[88:91], v[20:35]
	v_exp_f32_e32 v80, v80
	v_exp_f32_e32 v81, v81
	v_exp_f32_e32 v82, v82
	v_exp_f32_e32 v83, v83
	s_waitcnt lgkmcnt(6)
	v_mfma_f32_32x32x16_bf16 v[4:19], v[152:155], v[104:107], v[4:19]
	v_exp_f32_e32 v36, v36
	v_exp_f32_e32 v37, v37
	v_exp_f32_e32 v38, v38
	v_exp_f32_e32 v39, v39
	s_waitcnt lgkmcnt(4)
	v_mfma_f32_32x32x16_bf16 v[20:35], v[152:155], v[52:55], v[20:35]
	v_exp_f32_e32 v40, v40
	v_exp_f32_e32 v41, v41
	v_exp_f32_e32 v42, v42
	v_exp_f32_e32 v43, v43
	s_waitcnt lgkmcnt(2)
	v_mfma_f32_32x32x16_bf16 v[4:19], v[148:151], v[56:59], v[4:19]
	v_exp_f32_e32 v44, v44
	v_exp_f32_e32 v45, v45
	v_exp_f32_e32 v46, v46
	v_exp_f32_e32 v47, v47
	s_waitcnt lgkmcnt(0)
	v_mfma_f32_32x32x16_bf16 v[20:35], v[148:151], v[60:63], v[20:35]
	v_exp_f32_e32 v48, v48
	v_exp_f32_e32 v49, v49
	v_exp_f32_e32 v50, v50
	v_exp_f32_e32 v51, v51
	v_add_f32_e32 v52, v68, v69
	v_add_f32_e32 v52, v70, v52
	v_add_f32_e32 v52, v71, v52
	v_add_f32_e32 v52, v72, v52
	v_add_f32_e32 v52, v73, v52
	v_add_f32_e32 v52, v74, v52
	v_add_f32_e32 v52, v75, v52
	v_add_f32_e32 v52, v76, v52
	v_add_f32_e32 v52, v77, v52
	v_add_f32_e32 v52, v78, v52
	v_add_f32_e32 v52, v79, v52
	v_add_f32_e32 v52, v80, v52
	v_add_f32_e32 v52, v81, v52
	v_add_f32_e32 v52, v82, v52
	v_add_f32_e32 v52, v83, v52
	v_add_f32_e32 v52, v36, v52
	v_add_f32_e32 v52, v37, v52
	v_add_f32_e32 v52, v38, v52
	v_add_f32_e32 v52, v39, v52
	v_add_f32_e32 v52, v40, v52
	v_add_f32_e32 v52, v41, v52
	v_add_f32_e32 v52, v42, v52
	v_add_f32_e32 v52, v43, v52
	v_add_f32_e32 v52, v44, v52
	v_add_f32_e32 v52, v45, v52
	v_add_f32_e32 v52, v46, v52
	v_add_f32_e32 v52, v47, v52
	v_add_f32_e32 v52, v48, v52
	v_add_f32_e32 v52, v49, v52
	v_add_f32_e32 v52, v50, v52
	v_add_f32_e32 v52, v51, v52
	v_add_f32_e32 v3, v3, v52
	v_cvt_pk_bf16_f32 v36, v36, v37
	v_cvt_pk_bf16_f32 v52, v68, v69
	v_cvt_pk_bf16_f32 v53, v70, v71
	v_cvt_pk_bf16_f32 v54, v72, v73
	v_cvt_pk_bf16_f32 v55, v74, v75
	v_cvt_pk_bf16_f32 v56, v76, v77
	v_cvt_pk_bf16_f32 v57, v78, v79
	v_cvt_pk_bf16_f32 v58, v80, v81
	v_cvt_pk_bf16_f32 v59, v82, v83
	v_cvt_pk_bf16_f32 v37, v38, v39
	v_cvt_pk_bf16_f32 v38, v40, v41
	v_cvt_pk_bf16_f32 v39, v42, v43
	v_cvt_pk_bf16_f32 v40, v44, v45
	v_cvt_pk_bf16_f32 v41, v46, v47
	v_cvt_pk_bf16_f32 v42, v48, v49
	v_cvt_pk_bf16_f32 v43, v50, v51
	v_add_u32_e32 v44, s5, v184
	v_add3_u32 v72, v44, v185, v186
	ds_read_b64_tr_b16 v[44:45],v72 offset:0
	ds_read_b64_tr_b16 v[46:47],v72 offset:512
	ds_read_b64_tr_b16 v[48:49],v72 offset:1024
	ds_read_b64_tr_b16 v[50:51],v72 offset:1536
	ds_read_b64_tr_b16 v[60:61],v72 offset:2048
	ds_read_b64_tr_b16 v[62:63],v72 offset:2560
	ds_read_b64_tr_b16 v[64:65],v72 offset:3072
	ds_read_b64_tr_b16 v[66:67],v72 offset:3584
	s_waitcnt lgkmcnt(0)
	s_nop 0
	v_mfma_f32_32x32x16_bf16 v[4:19], v[52:55], v[44:47], v[4:19]
	ds_read_b64_tr_b16 v[44:45],v72 offset:4096
	ds_read_b64_tr_b16 v[46:47],v72 offset:4608
	v_mfma_f32_32x32x16_bf16 v[4:19], v[56:59], v[48:51], v[4:19]
	ds_read_b64_tr_b16 v[48:49],v72 offset:5120
	ds_read_b64_tr_b16 v[50:51],v72 offset:5632
	v_mfma_f32_32x32x16_bf16 v[4:19], v[36:39], v[60:63], v[4:19]
	ds_read_b64_tr_b16 v[60:61],v72 offset:6144
	ds_read_b64_tr_b16 v[62:63],v72 offset:6656
	ds_read_b64_tr_b16 v[68:69],v72 offset:7168
	ds_read_b64_tr_b16 v[70:71],v72 offset:7680
	s_waitcnt lgkmcnt(0)
	v_mfma_f32_32x32x16_bf16 v[4:19], v[40:43], v[64:67], v[4:19]
	v_mfma_f32_32x32x16_bf16 v[20:35], v[52:55], v[44:47], v[20:35]
	v_cmp_gt_u32_e32 vcc, 32, v202
	v_mfma_f32_32x32x16_bf16 v[20:35], v[56:59], v[48:51], v[20:35]
	v_mfma_f32_32x32x16_bf16 v[20:35], v[36:39], v[60:63], v[20:35]
	v_mov_b32_e32 v36, v3
	s_nop 1
	v_permlane32_swap_b32_e32 v3, v36
	v_mfma_f32_32x32x16_bf16 v[20:35], v[40:43], v[68:71], v[20:35]
	s_and_saveexec_b64 s[0:1], vcc
	v_add_f32_e32 v3, v3, v36
	v_lshl_add_u32 v36, v204, 2, s4
	ds_write_b32 v36, v3 offset:49280
	s_or_b64 exec, exec, s[0:1]
	s_waitcnt lgkmcnt(0)
	v_lshl_add_u32 v3, v205, 4, s4
	ds_read_b128 v[36:39], v3 offset:49280
	ds_read_b128 v[40:43], v3 offset:49312
	s_lshl_b32 s0, s10, 5
	s_add_i32 s0, s23, s0
	s_mul_hi_u32 s1, s0, 0x600
	s_waitcnt lgkmcnt(1)
	v_rcp_f32_e32 v44, v36
	v_rcp_f32_e32 v45, v37
	v_rcp_f32_e32 v46, v38
	v_rcp_f32_e32 v47, v39
	s_waitcnt lgkmcnt(0)
	v_rcp_f32_e32 v48, v40
	ds_read_b128 v[36:39], v3 offset:49344
	v_rcp_f32_e32 v49, v41
	v_rcp_f32_e32 v50, v42
	v_rcp_f32_e32 v51, v43
	ds_read_b128 v[40:43], v3 offset:49376
	s_mulk_i32 s0, 0x600
	s_add_u32 s0, s18, s0
	s_addc_u32 s1, s19, s1
	s_lshl_b32 s2, s10, 12
	s_waitcnt lgkmcnt(1)
	v_rcp_f32_e32 v3, v36
	v_rcp_f32_e32 v36, v37
	v_rcp_f32_e32 v37, v38
	v_rcp_f32_e32 v38, v39
	s_waitcnt lgkmcnt(0)
	v_rcp_f32_e32 v39, v40
	v_rcp_f32_e32 v40, v41
	v_rcp_f32_e32 v41, v42
	v_rcp_f32_e32 v42, v43
	s_add_i32 s2, s2, 0
	v_lshlrev_b32_e32 v43, 9, v205
	v_lshlrev_b32_e32 v52, 1, v204
	v_mul_f32_e32 v4, v4, v44
	v_add3_u32 v43, s2, v43, v52
	v_cvt_pk_bf16_f32 v4, v4, s0
	ds_write_b16 v43, v4 offset:51200
	v_mul_f32_e32 v4, v20, v44
	v_cvt_pk_bf16_f32 v4, v4, s0
	ds_write_b16 v43, v4 offset:51264
	v_mul_f32_e32 v4, v5, v45
	v_cvt_pk_bf16_f32 v4, v4, s0
	ds_write_b16 v43, v4 offset:51328
	v_mul_f32_e32 v4, v21, v45
	v_cvt_pk_bf16_f32 v4, v4, s0
	ds_write_b16 v43, v4 offset:51392
	v_mul_f32_e32 v4, v6, v46
	v_cvt_pk_bf16_f32 v4, v4, s0
	ds_write_b16 v43, v4 offset:51456
	v_mul_f32_e32 v4, v22, v46
	v_cvt_pk_bf16_f32 v4, v4, s0
	ds_write_b16 v43, v4 offset:51520
	v_mul_f32_e32 v4, v7, v47
	v_cvt_pk_bf16_f32 v4, v4, s0
	ds_write_b16 v43, v4 offset:51584
	v_mul_f32_e32 v4, v23, v47
	v_cvt_pk_bf16_f32 v4, v4, s0
	ds_write_b16 v43, v4 offset:51648
	v_mul_f32_e32 v4, v8, v48
	v_cvt_pk_bf16_f32 v4, v4, s0
	ds_write_b16 v43, v4 offset:52224
	v_mul_f32_e32 v4, v24, v48
	v_cvt_pk_bf16_f32 v4, v4, s0
	ds_write_b16 v43, v4 offset:52288
	v_mul_f32_e32 v4, v9, v49
	v_cvt_pk_bf16_f32 v4, v4, s0
	ds_write_b16 v43, v4 offset:52352
	v_mul_f32_e32 v4, v25, v49
	v_cvt_pk_bf16_f32 v4, v4, s0
	ds_write_b16 v43, v4 offset:52416
	v_mul_f32_e32 v4, v10, v50
	v_cvt_pk_bf16_f32 v4, v4, s0
	ds_write_b16 v43, v4 offset:52480
	v_mul_f32_e32 v4, v26, v50
	v_cvt_pk_bf16_f32 v4, v4, s0
	ds_write_b16 v43, v4 offset:52544
	v_mul_f32_e32 v4, v11, v51
	v_cvt_pk_bf16_f32 v4, v4, s0
	ds_write_b16 v43, v4 offset:52608
	v_mul_f32_e32 v4, v27, v51
	v_cvt_pk_bf16_f32 v4, v4, s0
	ds_write_b16 v43, v4 offset:52672
	v_mul_f32_e32 v4, v12, v3
	v_mul_f32_e32 v3, v28, v3
	v_cvt_pk_bf16_f32 v3, v3, s0
	ds_write_b16 v43, v3 offset:53312
	v_mul_f32_e32 v3, v13, v36
	v_cvt_pk_bf16_f32 v3, v3, s0
	ds_write_b16 v43, v3 offset:53376
	v_mul_f32_e32 v3, v29, v36
	v_cvt_pk_bf16_f32 v3, v3, s0
	ds_write_b16 v43, v3 offset:53440
	v_mul_f32_e32 v3, v14, v37
	v_cvt_pk_bf16_f32 v3, v3, s0
	ds_write_b16 v43, v3 offset:53504
	v_mul_f32_e32 v3, v30, v37
	v_cvt_pk_bf16_f32 v3, v3, s0
	ds_write_b16 v43, v3 offset:53568
	v_mul_f32_e32 v3, v15, v38
	v_cvt_pk_bf16_f32 v3, v3, s0
	ds_write_b16 v43, v3 offset:53632
	v_mul_f32_e32 v3, v31, v38
	v_cvt_pk_bf16_f32 v3, v3, s0
	ds_write_b16 v43, v3 offset:53696
	v_mul_f32_e32 v3, v16, v39
	v_cvt_pk_bf16_f32 v3, v3, s0
	ds_write_b16 v43, v3 offset:54272
	v_mul_f32_e32 v3, v32, v39
	v_cvt_pk_bf16_f32 v3, v3, s0
	ds_write_b16 v43, v3 offset:54336
	v_mul_f32_e32 v3, v17, v40
	v_cvt_pk_bf16_f32 v3, v3, s0
	ds_write_b16 v43, v3 offset:54400
	v_mul_f32_e32 v3, v33, v40
	v_cvt_pk_bf16_f32 v3, v3, s0
	ds_write_b16 v43, v3 offset:54464
	v_mul_f32_e32 v3, v18, v41
	v_cvt_pk_bf16_f32 v3, v3, s0
	ds_write_b16 v43, v3 offset:54528
	v_mul_f32_e32 v3, v34, v41
	v_cvt_pk_bf16_f32 v3, v3, s0
	ds_write_b16 v43, v3 offset:54592
	v_mul_f32_e32 v3, v19, v42
	v_cvt_pk_bf16_f32 v3, v3, s0
	ds_write_b16 v43, v3 offset:54656
	v_mul_f32_e32 v3, v35, v42
	v_cvt_pk_bf16_f32 v4, v4, s0
	v_cvt_pk_bf16_f32 v3, v3, s0
	ds_write_b16 v43, v4 offset:53248
	ds_write_b16 v43, v3 offset:54720
	v_lshrrev_b32_e32 v3, 3, v202
	v_and_b32_e32 v4, 56, v203
	s_lshl_b32 s3, s22, 1
	v_lshlrev_b32_e32 v8, 1, v4
	v_lshlrev_b32_e32 v4, 7, v3
	s_add_u32 s0, s0, s3
	s_waitcnt lgkmcnt(0)
	v_add3_u32 v16, s2, v8, v4
	s_addc_u32 s1, s1, 0
	v_mov_b32_e32 v9, 0
	ds_read_b128 v[4:7], v16 offset:51200
	v_mul_u32_u24_e32 v3, 0x300, v3
	v_lshl_add_u64 v[10:11], s[0:1], 0, v[8:9]
	v_lshlrev_b32_e32 v8, 1, v3
	v_lshl_add_u64 v[12:13], v[10:11], 0, v[8:9]
	ds_read_b128 v[8:11], v16 offset:52224
	s_movk_i32 s0, 0x3000
	s_waitcnt lgkmcnt(1)
	global_store_dwordx4 v[12:13], v[4:7], off
	s_nop 1
	v_add_co_u32_e32 v4, vcc, s0, v12
	s_nop 1
	v_addc_co_u32_e32 v5, vcc, 0, v13, vcc
	s_waitcnt lgkmcnt(0)
	global_store_dwordx4 v[4:5], v[8:11], off
	ds_read_b128 v[4:7], v16 offset:53248
	ds_read_b128 v[8:11], v16 offset:54272
	v_add_co_u32_e32 v14, vcc, 0x6000, v12
	s_nop 1
	v_addc_co_u32_e32 v15, vcc, 0, v13, vcc
	s_waitcnt lgkmcnt(1)
	global_store_dwordx4 v[14:15], v[4:7], off
	s_nop 1
	v_add_co_u32_e32 v4, vcc, 0x9000, v12
	s_nop 1
	v_addc_co_u32_e32 v5, vcc, 0, v13, vcc
	s_waitcnt lgkmcnt(0)
	global_store_dwordx4 v[4:5], v[8:11], off
	s_waitcnt lgkmcnt(0)
	s_barrier
	s_branch .LBB1_37
